# conversion tickets now 4 tiles: second pair's loads issued before first pair's second store step (register-renamed copies, SGPR state saved in lanes)
# baseline (speedup 1.0000x reference)
; #define LAS __attribute__((address_space(3)))
; __device__ __forceinline__ CvTile cv_decode(const Ptrs& P, int it) {
;     constexpr int T_IN = (D / 128) * (NQKV / 256), T_O = (D / 128) * (D / 256), T_G = (D / 128) * (FF / 256), T_D = (FF / 128) * (D / 256), T_E = 2 * T_G + T_D;
;     CvTile c; int r = it; c.gain = nullptr; c.pitch = 0;
;     if (r < T_IN) { c.W = P.w_in; c.WT = (unsigned char*)P.Wqkv_t; c.K = D; c.N = NQKV; c.mode = 0; c.f8 = 0; c.r = r; return c; } r -= T_IN;
;     if (r < T_O) { c.W = P.w_out; c.WT = (unsigned char*)P.Wo_t; c.K = D; c.N = D; c.mode = 0; c.f8 = (WO8_LAYER == 0) ? 1 : 0; c.r = r; return c; } r -= T_O;
;     if (r < T_G) { c.W = P.dwg; c.WT = P.Wgu_d; c.K = D; c.N = FF; c.mode = 1; c.f8 = 1; c.r = r; return c; } r -= T_G;
;     if (r < T_G) { c.W = P.dwu; c.WT = P.Wgu_d; c.K = D; c.N = FF; c.mode = 2; c.f8 = 1; c.r = r; return c; } r -= T_G;
;     if (r < T_D) { c.W = P.dwd; c.WT = P.Wd_d; c.K = FF; c.N = D; c.mode = 0; c.f8 = 1; c.r = r; return c; } r -= T_D;
;     if (r < T_IN) { const int kb = r / 24, nb = r - kb * 24; c.K = D; c.mode = 0; c.pitch = NQKV; c.gain = P.attn_norm + D;
;         c.W = P.w_in + (size_t)D * NQKV; c.WT = P.Wv8; c.N = NQKV; c.f8 = 1; c.r = kb * 24 + nb;
;         return c; } r -= T_IN;
;     if (r < T_O) { c.W = P.w_out + (size_t)D * D; c.WT = (unsigned char*)(P.Wo_t + (size_t)D * D); c.K = D; c.N = D; c.mode = 0; c.f8 = (WO8_LAYER == 1) ? 1 : 0; c.r = r; return c; } r -= T_O;
;     const int e = r / T_E; r -= e * T_E; c.f8 = 1;
;     if (r < T_G) { c.W = P.mwg + (size_t)e * D * FF; c.WT = P.Wgu_m + (size_t)e * NGU * D; c.K = D; c.N = FF; c.mode = 1; c.r = r; return c; } r -= T_G;
;     if (r < T_G) { c.W = P.mwu + (size_t)e * D * FF; c.WT = P.Wgu_m + (size_t)e * NGU * D; c.K = D; c.N = FF; c.mode = 2; c.r = r; return c; } r -= T_G;
;     c.W = P.mwd + (size_t)e * FF * D; c.WT = P.Wd_m + (size_t)e * D * FF; c.K = FF; c.N = D; c.mode = 0; c.r = r; return c;
; __device__ __forceinline__ void attn_conv_phase(const Ptrs& P, const att::AttnArgs& A, int layer, unsigned* qctr, unsigned char* lds, const int wave_) {
;     ...
;             const int t0 = CV_L0 + (layer * att::N_CHUNKS + (code & 0x7fff)) * att::CHUNK_TILES;
;             convert_weights(P, (LAS unsigned char*)lds, t0, 1, t0 + att::CHUNK_TILES, wave_, lane_id());
.LBB0_489:
	v_writelane_b32 v150, s0, 0
	v_writelane_b32 v150, s1, 1
	v_writelane_b32 v150, s2, 2
	v_writelane_b32 v150, s14, 3
	v_writelane_b32 v150, s16, 4
	v_writelane_b32 v150, s17, 5
	v_writelane_b32 v150, s18, 6
	v_writelane_b32 v150, s19, 7
	v_writelane_b32 v150, s22, 8
	v_writelane_b32 v150, s23, 9
	v_writelane_b32 v150, s27, 10
	v_writelane_b32 v150, s28, 11
	v_writelane_b32 v150, s29, 12
	v_writelane_b32 v150, s30, 13
	v_writelane_b32 v150, s40, 14
	v_writelane_b32 v150, s41, 15
	v_writelane_b32 v150, s42, 16
	v_writelane_b32 v150, s43, 17
	v_writelane_b32 v150, s44, 18
	v_writelane_b32 v150, s45, 19
	v_writelane_b32 v150, s46, 20
	v_writelane_b32 v150, s47, 21
	v_writelane_b32 v150, s56, 22
	v_writelane_b32 v150, s66, 23
	v_writelane_b32 v150, s67, 24
	v_writelane_b32 v150, s68, 25
	v_writelane_b32 v150, s69, 26
	v_writelane_b32 v150, s72, 27
	v_writelane_b32 v150, s73, 28
	v_writelane_b32 v150, s76, 29
	v_writelane_b32 v150, s77, 30
	v_writelane_b32 v150, s84, 31
	v_writelane_b32 v150, s85, 32
	s_and_b32 s15, s26, 0x7fff
	s_mul_i32 s0, s80, 0x420
	s_add_i32 s15, s15, s0
	s_lshl_b32 s15, s15, 1
	s_add_i32 s15, s15, 1
	s_lshl_b32 s14, s15, 1
	s_cmpk_gt_u32 s15, 0xbf
	v_mbcnt_lo_u32_b32 v132, -1, 0
	v_mbcnt_hi_u32_b32 v132, -1, v132
	s_cselect_b64 s[42:43], -1, 0
	s_cmpk_lt_u32 s15, 0xc0
	s_mov_b64 s[28:29], -1
	s_cbranch_scc1 .Lpc_460
	s_cmpk_gt_u32 s15, 0xff
	s_mov_b64 s[0:1], -1
	s_cbranch_scc0 .Lpc_458
	s_add_i32 s0, s14, 0xfffffe00
	s_mul_hi_u32 s1, s0, 0x3e0f83e1
	s_lshr_b32 s23, s1, 8
	s_mul_i32 s22, s23, 0xfffffbe0
	s_add_i32 s22, s22, s0
	s_cmpk_gt_i32 s22, 0x15f
	s_mul_hi_u32 s27, s23, 0x2c00000
	s_mul_i32 s30, s23, 0x2c00000
	s_mov_b64 s[0:1], -1
	s_cbranch_scc0 .Lpc_455
	s_mov_b64 s[72:73], -1
	s_cmpk_gt_u32 s22, 0x2bf
	s_cbranch_scc0 .Lpc_453
	s_add_i32 s18, s22, 0xfffffd40
	v_readlane_b32 s0, v254, 49
	v_readlane_b32 s1, v254, 50
	s_add_u32 s46, s0, s30
	s_addc_u32 s47, s1, s27
	s_mul_i32 s1, s23, 0xb00000
	v_readlane_b32 s2, v254, 58
	s_mul_hi_u32 s0, s23, 0xb00000
	s_add_u32 s66, s2, s1
	v_readlane_b32 s1, v254, 59
	s_addc_u32 s67, s1, s0
	s_mov_b64 s[0:1], 0

; __device__ __forceinline__ CvTile cv_decode(const Ptrs& P, int it) {
;     ...
;     const int e = r / T_E; r -= e * T_E; c.f8 = 1;
;     if (r < T_G) { c.W = P.mwg + (size_t)e * D * FF; c.WT = P.Wgu_m + (size_t)e * NGU * D; c.K = D; c.N = FF; c.mode = 1; c.r = r; return c; } r -= T_G;
;     if (r < T_G) { c.W = P.mwu + (size_t)e * D * FF; c.WT = P.Wgu_m + (size_t)e * NGU * D; c.K = D; c.N = FF; c.mode = 2; c.r = r; return c; } r -= T_G;
;     c.W = P.mwd + (size_t)e * FF * D; c.WT = P.Wd_m + (size_t)e * D * FF; c.K = FF; c.N = D; c.mode = 0; c.r = r; return c;
.Lpc_461:
	s_lshr_b32 s0, s44, 8
	v_cvt_f32_u32_e32 v134, s0
	s_sub_i32 s23, 0, s0
	s_abs_i32 s22, s18
	s_ashr_i32 s1, s18, 31
	v_rcp_iflag_f32_e32 v134, v134
	v_lshlrev_b32_e32 v136, 2, v132
	v_ashrrev_i32_e32 v137, 31, v136
	s_mov_b32 s45, s90
	v_mul_f32_e32 v134, 0x4f7ffffe, v134
	v_cvt_u32_f32_e32 v134, v134
	s_nop 0
	v_readfirstlane_b32 s27, v134
	s_mul_i32 s23, s23, s27
	s_mul_hi_u32 s23, s27, s23
	s_add_i32 s27, s27, s23
	s_mul_hi_u32 s23, s22, s27
	s_mul_i32 s27, s23, s0
	s_sub_i32 s22, s22, s27
	s_add_i32 s27, s23, 1
	s_sub_i32 s30, s22, s0
	s_cmp_ge_u32 s22, s0
	s_cselect_b32 s23, s27, s23
	s_cselect_b32 s22, s30, s22
	s_add_i32 s27, s23, 1
	s_cmp_ge_u32 s22, s0
	s_cselect_b32 s22, s27, s23
	s_xor_b32 s22, s22, s1
	s_sub_i32 s1, s22, s1
	s_lshl_b32 s56, s1, 7
	s_mul_i32 s0, s1, s0
	s_add_i32 s1, s56, s96
	s_sub_i32 s0, s18, s0
	s_ashr_i32 s18, s1, 31
	s_mul_i32 s18, s18, s44
	s_mul_hi_u32 s22, s1, s44
	s_add_i32 s23, s22, s18
	s_mul_i32 s22, s1, s44
	s_lshl_b64 s[22:23], s[22:23], 2
	s_add_u32 s18, s46, s22
	s_addc_u32 s22, s47, s23
	s_lshl_b32 s84, s0, 8
	s_ashr_i32 s85, s84, 31
	s_lshl_b64 s[0:1], s[84:85], 2
	s_add_u32 s0, s18, s0
	s_addc_u32 s1, s22, s1
	v_lshl_add_u64 v[138:139], v[136:137], 2, s[0:1]
	v_lshl_add_u64 v[140:141], s[44:45], 2, v[138:139]
	s_lshl_b32 s0, s44, 1
	s_mov_b32 s1, s90
	global_load_dwordx4 v[156:159], v[138:139], off nt
	global_load_dwordx4 v[160:163], v[140:141], off nt
	v_lshl_add_u64 v[140:141], s[0:1], 2, v[138:139]
	s_mul_i32 s0, s44, 3
	global_load_dwordx4 v[164:167], v[140:141], off nt
	v_lshl_add_u64 v[140:141], s[0:1], 2, v[138:139]
	s_lshl_b32 s0, s44, 2
	global_load_dwordx4 v[168:171], v[140:141], off nt
	v_lshl_add_u64 v[140:141], s[0:1], 2, v[138:139]
	s_mul_i32 s0, s44, 5
	global_load_dwordx4 v[172:175], v[140:141], off nt
	v_lshl_add_u64 v[140:141], s[0:1], 2, v[138:139]
	s_mul_i32 s0, s44, 6
	global_load_dwordx4 v[176:179], v[140:141], off nt
	v_lshl_add_u64 v[140:141], s[0:1], 2, v[138:139]
	s_mul_i32 s0, s44, 7
	global_load_dwordx4 v[180:183], v[140:141], off nt
	v_lshl_add_u64 v[140:141], s[0:1], 2, v[138:139]
	s_lshl_b32 s0, s44, 3
	global_load_dwordx4 v[184:187], v[140:141], off nt
	v_lshl_add_u64 v[140:141], s[0:1], 2, v[138:139]
	s_mul_i32 s0, s44, 9
	global_load_dwordx4 v[208:211], v[140:141], off nt
	v_lshl_add_u64 v[140:141], s[0:1], 2, v[138:139]
	s_mul_i32 s0, s44, 10
	global_load_dwordx4 v[212:215], v[140:141], off nt
	v_lshl_add_u64 v[140:141], s[0:1], 2, v[138:139]
	s_mul_i32 s0, s44, 11
	global_load_dwordx4 v[216:219], v[140:141], off nt
	v_lshl_add_u64 v[140:141], s[0:1], 2, v[138:139]
	s_mul_i32 s0, s44, 12
	global_load_dwordx4 v[220:223], v[140:141], off nt
	v_lshl_add_u64 v[140:141], s[0:1], 2, v[138:139]
	s_mul_i32 s0, s44, 13
	global_load_dwordx4 v[224:227], v[140:141], off nt
	v_lshl_add_u64 v[140:141], s[0:1], 2, v[138:139]
	s_mul_i32 s0, s44, 14
	global_load_dwordx4 v[228:231], v[140:141], off nt
	v_lshl_add_u64 v[140:141], s[0:1], 2, v[138:139]
	s_mul_i32 s0, s44, 15
	v_lshl_add_u64 v[138:139], s[0:1], 2, v[138:139]
	global_load_dwordx4 v[232:235], v[140:141], off nt
	global_load_dwordx4 v[236:239], v[138:139], off nt
	s_branch .Lpipe_xc_done

.Lpipe_xc_done:
	v_writelane_b32 v151, s0, 0
	v_writelane_b32 v151, s1, 1
	v_writelane_b32 v151, s2, 2
	v_writelane_b32 v151, s14, 3
	v_writelane_b32 v151, s16, 4
	v_writelane_b32 v151, s17, 5
	v_writelane_b32 v151, s18, 6
	v_writelane_b32 v151, s19, 7
	v_writelane_b32 v151, s22, 8
	v_writelane_b32 v151, s23, 9
	v_writelane_b32 v151, s27, 10
	v_writelane_b32 v151, s28, 11
	v_writelane_b32 v151, s29, 12
	v_writelane_b32 v151, s30, 13
	v_writelane_b32 v151, s40, 14
	v_writelane_b32 v151, s41, 15
	v_writelane_b32 v151, s42, 16
	v_writelane_b32 v151, s43, 17
	v_writelane_b32 v151, s44, 18
	v_writelane_b32 v151, s45, 19
	v_writelane_b32 v151, s46, 20
	v_writelane_b32 v151, s47, 21
	v_writelane_b32 v151, s56, 22
	v_writelane_b32 v151, s66, 23
	v_writelane_b32 v151, s67, 24
	v_writelane_b32 v151, s68, 25
	v_writelane_b32 v151, s69, 26
	v_writelane_b32 v151, s72, 27
	v_writelane_b32 v151, s73, 28
	v_writelane_b32 v151, s76, 29
	v_writelane_b32 v151, s77, 30
	v_writelane_b32 v151, s84, 31
	v_writelane_b32 v151, s85, 32
	v_readlane_b32 s0, v150, 0
	v_readlane_b32 s1, v150, 1
	v_readlane_b32 s2, v150, 2
	v_readlane_b32 s14, v150, 3
	v_readlane_b32 s16, v150, 4
	v_readlane_b32 s17, v150, 5
	v_readlane_b32 s18, v150, 6
	v_readlane_b32 s19, v150, 7
	v_readlane_b32 s22, v150, 8
	v_readlane_b32 s23, v150, 9
	v_readlane_b32 s27, v150, 10
	v_readlane_b32 s28, v150, 11
	v_readlane_b32 s29, v150, 12
	v_readlane_b32 s30, v150, 13
	v_readlane_b32 s40, v150, 14
	v_readlane_b32 s41, v150, 15
	v_readlane_b32 s42, v150, 16
	v_readlane_b32 s43, v150, 17
	v_readlane_b32 s44, v150, 18
	v_readlane_b32 s45, v150, 19
	v_readlane_b32 s46, v150, 20
	v_readlane_b32 s47, v150, 21
	v_readlane_b32 s56, v150, 22
	v_readlane_b32 s66, v150, 23
	v_readlane_b32 s67, v150, 24
	v_readlane_b32 s68, v150, 25
	v_readlane_b32 s69, v150, 26
	v_readlane_b32 s72, v150, 27
	v_readlane_b32 s73, v150, 28
	v_readlane_b32 s76, v150, 29
	v_readlane_b32 s77, v150, 30
	v_readlane_b32 s84, v150, 31
	v_readlane_b32 s85, v150, 32
	s_nop 4
.Lpb1_489:
	v_readlane_b32 s78, v255, 22
	s_cmp_eq_u64 s[28:29], 0
	v_readlane_b32 s68, v254, 36
	s_movk_i32 s66, 0xb00
	v_readlane_b32 s2, v254, 45
	v_readlane_b32 s79, v255, 23
	v_readlane_b32 s69, v254, 37
	s_cbranch_scc1 .Lpb1_491
	s_ashr_i32 s71, s70, 31
	s_lshl_b64 s[0:1], s[70:71], 2
	s_add_u32 s0, s28, s0
	s_addc_u32 s1, s29, s1
	s_lshl_b32 s14, s96, 2
	s_load_dwordx16 s[40:55], s[0:1], s14 offset:0x0
	s_waitcnt lgkmcnt(0)
	s_mov_b32 s0, s43
	s_waitcnt vmcnt(28)
	v_pk_mul_f32 v[16:17], v[16:17], s[0:1] op_sel_hi:[1,0]
	v_pk_mul_f32 v[14:15], v[14:15], s[0:1] op_sel_hi:[1,0]
	s_mov_b32 s0, s45
	s_waitcnt vmcnt(26)
	v_pk_mul_f32 v[24:25], v[24:25], s[0:1] op_sel_hi:[1,0]
	v_pk_mul_f32 v[22:23], v[22:23], s[0:1] op_sel_hi:[1,0]
	s_mov_b32 s0, s47
	s_waitcnt vmcnt(24)
	v_pk_mul_f32 v[32:33], v[32:33], s[0:1] op_sel_hi:[1,0]
	v_pk_mul_f32 v[30:31], v[30:31], s[0:1] op_sel_hi:[1,0]
	s_mov_b32 s0, s49
	s_waitcnt vmcnt(22)
	v_pk_mul_f32 v[40:41], v[40:41], s[0:1] op_sel_hi:[1,0]
	v_pk_mul_f32 v[38:39], v[38:39], s[0:1] op_sel_hi:[1,0]
	s_mov_b32 s0, s51
	s_waitcnt vmcnt(20)
	v_pk_mul_f32 v[48:49], v[48:49], s[0:1] op_sel_hi:[1,0]
	v_pk_mul_f32 v[46:47], v[46:47], s[0:1] op_sel_hi:[1,0]
	s_mov_b32 s0, s53
	s_waitcnt vmcnt(18)
	v_pk_mul_f32 v[56:57], v[56:57], s[0:1] op_sel_hi:[1,0]
	v_pk_mul_f32 v[54:55], v[54:55], s[0:1] op_sel_hi:[1,0]
	s_mov_b32 s0, s55
	v_pk_mul_f32 v[4:5], v[4:5], s[40:41] op_sel_hi:[1,0]
	v_pk_mul_f32 v[2:3], v[2:3], s[40:41] op_sel_hi:[1,0]
	v_pk_mul_f32 v[8:9], v[8:9], s[40:41] op_sel:[0,1]
	v_pk_mul_f32 v[6:7], v[6:7], s[40:41] op_sel:[0,1]
	v_pk_mul_f32 v[12:13], v[12:13], s[42:43] op_sel_hi:[1,0]
	v_pk_mul_f32 v[10:11], v[10:11], s[42:43] op_sel_hi:[1,0]
	v_pk_mul_f32 v[20:21], v[20:21], s[44:45] op_sel_hi:[1,0]
	v_pk_mul_f32 v[18:19], v[18:19], s[44:45] op_sel_hi:[1,0]
	v_pk_mul_f32 v[28:29], v[28:29], s[46:47] op_sel_hi:[1,0]
	v_pk_mul_f32 v[26:27], v[26:27], s[46:47] op_sel_hi:[1,0]
	v_pk_mul_f32 v[36:37], v[36:37], s[48:49] op_sel_hi:[1,0]
	v_pk_mul_f32 v[34:35], v[34:35], s[48:49] op_sel_hi:[1,0]
	v_pk_mul_f32 v[44:45], v[44:45], s[50:51] op_sel_hi:[1,0]
	v_pk_mul_f32 v[42:43], v[42:43], s[50:51] op_sel_hi:[1,0]
	v_pk_mul_f32 v[52:53], v[52:53], s[52:53] op_sel_hi:[1,0]
	v_pk_mul_f32 v[50:51], v[50:51], s[52:53] op_sel_hi:[1,0]
	s_waitcnt vmcnt(17)
	v_pk_mul_f32 v[60:61], v[60:61], s[54:55] op_sel_hi:[1,0]
	v_pk_mul_f32 v[58:59], v[58:59], s[54:55] op_sel_hi:[1,0]
	s_waitcnt vmcnt(16)
	v_pk_mul_f32 v[64:65], v[64:65], s[0:1] op_sel_hi:[1,0]
	v_pk_mul_f32 v[62:63], v[62:63], s[0:1] op_sel_hi:[1,0]
; __device__ __forceinline__ unsigned pk4_fp8(float a, float b, float c, float d) { int w = 0; w = __builtin_amdgcn_cvt_pk_fp8_f32(a, b, w, false); w = __builtin_amdgcn_cvt_pk_fp8_f32(c, d, w, true); return (unsigned)w; }
; #define LAS __attribute__((address_space(3)))
; #define lane (lane_id())
; __device__ __forceinline__ void cv8_to_lds(const f32x4 (&v)[16], LAS unsigned char* T, int wave, int lane) {
;     unsigned d[16];
; #pragma unroll
;     for (int i = 0; i < 16; ++i) d[i] = pg8::pk4_fp8(v[i].x * 256.f, v[i].y * 256.f, v[i].z * 256.f, v[i].w * 256.f);
;     unsigned o[4][4];
; #pragma unroll
;     for (int q = 0; q < 4; ++q) { const unsigned a = d[4 * q], b = d[4 * q + 1], c = d[4 * q + 2], e = d[4 * q + 3];
;         const unsigned t0 = __builtin_amdgcn_perm(b, a, 0x05010400u), t1 = __builtin_amdgcn_perm(b, a, 0x07030602u), t2 = __builtin_amdgcn_perm(e, c, 0x05010400u), t3 = __builtin_amdgcn_perm(e, c, 0x07030602u);
;         o[0][q] = __builtin_amdgcn_perm(t2, t0, 0x05040100u); o[1][q] = __builtin_amdgcn_perm(t2, t0, 0x07060302u); o[2][q] = __builtin_amdgcn_perm(t3, t1, 0x05040100u); o[3][q] = __builtin_amdgcn_perm(t3, t1, 0x07060302u); }
; #pragma unroll
;     for (int j = 0; j < 4; ++j) { v4u w; w.x = o[j][0]; w.y = o[j][1]; w.z = o[j][2]; w.w = o[j][3];
;         *(LAS v4u*)(T + (4 * lane + j) * 128 + 16 * (wave ^ (lane & 7))) = w; }
; }
.Lpb1_491:
	s_xor_b64 s[28:29], s[74:75], -1
	v_readlane_b32 s48, v254, 38
	v_readlane_b32 s50, v254, 40
	v_readlane_b32 s52, v254, 42
	v_readlane_b32 s53, v254, 43
	s_mov_b64 s[0:1], -1
	s_and_b64 vcc, exec, s[28:29]
	v_readlane_b32 s49, v254, 39
	v_readlane_b32 s51, v254, 41
	s_cbranch_vccz .Lpb1_495
	s_waitcnt vmcnt(31)
	v_mul_f32_e32 v67, 0x43800000, v2
	v_mul_f32_e32 v105, 0x43800000, v3
	v_mov_b32_e32 v108, v1
	v_cvt_pk_fp8_f32 v108, v67, v105
	s_waitcnt vmcnt(30)
	v_mul_f32_e32 v67, 0x43800000, v6
	v_mul_f32_e32 v105, 0x43800000, v7
	v_mov_b32_e32 v109, v1
	v_cvt_pk_fp8_f32 v109, v67, v105
	v_mul_f32_e32 v67, 0x43800000, v8
	v_mul_f32_e32 v105, 0x43800000, v9
	v_mov_b32_e32 v110, v1
	v_cvt_pk_fp8_f32 v109, v67, v105 op_sel:[0,0,1]
	s_waitcnt vmcnt(29)
	v_mul_f32_e32 v67, 0x43800000, v10
	v_mul_f32_e32 v105, 0x43800000, v11
	v_cvt_pk_fp8_f32 v110, v67, v105
	s_waitcnt vmcnt(28)
	v_mul_f32_e32 v67, 0x43800000, v14
	v_mul_f32_e32 v105, 0x43800000, v15
	v_mov_b32_e32 v111, v1
	v_cvt_pk_fp8_f32 v111, v67, v105
	v_mul_f32_e32 v67, 0x43800000, v16
	v_mul_f32_e32 v105, 0x43800000, v17
	v_mov_b32_e32 v112, v1
	v_cvt_pk_fp8_f32 v111, v67, v105 op_sel:[0,0,1]
	s_waitcnt vmcnt(27)
	v_mul_f32_e32 v67, 0x43800000, v18
	v_mul_f32_e32 v105, 0x43800000, v19
	v_cvt_pk_fp8_f32 v112, v67, v105
	s_waitcnt vmcnt(26)
	v_mul_f32_e32 v67, 0x43800000, v22
	v_mul_f32_e32 v105, 0x43800000, v23
	v_mov_b32_e32 v113, v1
	v_cvt_pk_fp8_f32 v113, v67, v105
	v_mul_f32_e32 v67, 0x43800000, v24
	v_mul_f32_e32 v105, 0x43800000, v25
	v_mov_b32_e32 v115, v1
	v_cvt_pk_fp8_f32 v113, v67, v105 op_sel:[0,0,1]
	s_waitcnt vmcnt(25)
	v_mul_f32_e32 v67, 0x43800000, v26
	v_mul_f32_e32 v105, 0x43800000, v27
	v_cvt_pk_fp8_f32 v115, v67, v105
	s_waitcnt vmcnt(24)
	v_mul_f32_e32 v67, 0x43800000, v30
	v_mul_f32_e32 v105, 0x43800000, v31
	v_mov_b32_e32 v116, v1
	v_cvt_pk_fp8_f32 v116, v67, v105
	v_mul_f32_e32 v67, 0x43800000, v32
	v_mul_f32_e32 v105, 0x43800000, v33
	v_mov_b32_e32 v117, v1
	v_cvt_pk_fp8_f32 v116, v67, v105 op_sel:[0,0,1]
	s_waitcnt vmcnt(23)
	v_mul_f32_e32 v67, 0x43800000, v34
	v_mul_f32_e32 v105, 0x43800000, v35
	v_cvt_pk_fp8_f32 v117, v67, v105
	s_waitcnt vmcnt(22)
	v_mul_f32_e32 v67, 0x43800000, v38
	v_mul_f32_e32 v105, 0x43800000, v39
	v_mov_b32_e32 v120, v1
	v_cvt_pk_fp8_f32 v120, v67, v105
	v_mul_f32_e32 v67, 0x43800000, v40
	v_mul_f32_e32 v105, 0x43800000, v41
	v_mov_b32_e32 v121, v1
	v_cvt_pk_fp8_f32 v120, v67, v105 op_sel:[0,0,1]
	s_waitcnt vmcnt(21)
	v_mul_f32_e32 v67, 0x43800000, v42
	v_mul_f32_e32 v105, 0x43800000, v43
	v_cvt_pk_fp8_f32 v121, v67, v105
	s_waitcnt vmcnt(20)
	v_mul_f32_e32 v67, 0x43800000, v46
	v_mul_f32_e32 v105, 0x43800000, v47
	v_mov_b32_e32 v122, v1
	v_cvt_pk_fp8_f32 v122, v67, v105
	v_mul_f32_e32 v67, 0x43800000, v48
	v_mul_f32_e32 v105, 0x43800000, v49
	v_mov_b32_e32 v123, v1
	v_cvt_pk_fp8_f32 v122, v67, v105 op_sel:[0,0,1]
	s_waitcnt vmcnt(19)
	v_mul_f32_e32 v67, 0x43800000, v50
	v_mul_f32_e32 v105, 0x43800000, v51
	v_cvt_pk_fp8_f32 v123, v67, v105
	s_waitcnt vmcnt(18)
	v_mul_f32_e32 v67, 0x43800000, v54
	v_mul_f32_e32 v105, 0x43800000, v55
	v_mov_b32_e32 v124, v1
	v_cvt_pk_fp8_f32 v124, v67, v105
	v_mul_f32_e32 v106, 0x43800000, v4
	v_mul_f32_e32 v107, 0x43800000, v5
	v_cvt_pk_fp8_f32 v108, v106, v107 op_sel:[0,0,1]
	v_mul_f32_e32 v106, 0x43800000, v12
	v_mul_f32_e32 v107, 0x43800000, v13
	v_mul_f32_e32 v67, 0x43800000, v56
	v_mul_f32_e32 v105, 0x43800000, v57
	v_cvt_pk_fp8_f32 v110, v106, v107 op_sel:[0,0,1]
	v_mul_f32_e32 v106, 0x43800000, v20
	v_mul_f32_e32 v107, 0x43800000, v21
	v_cvt_pk_fp8_f32 v124, v67, v105 op_sel:[0,0,1]
	s_waitcnt vmcnt(17)
	v_mul_f32_e32 v67, 0x43800000, v58
	v_mul_f32_e32 v105, 0x43800000, v59
	v_mov_b32_e32 v125, v1
	v_cvt_pk_fp8_f32 v112, v106, v107 op_sel:[0,0,1]
	v_mul_f32_e32 v106, 0x43800000, v28
	v_mul_f32_e32 v107, 0x43800000, v29
	v_cvt_pk_fp8_f32 v125, v67, v105
	s_waitcnt vmcnt(16)
	v_mul_f32_e32 v67, 0x43800000, v62
	v_mul_f32_e32 v105, 0x43800000, v63
	v_mov_b32_e32 v126, v1
	v_cvt_pk_fp8_f32 v115, v106, v107 op_sel:[0,0,1]
	v_mul_f32_e32 v106, 0x43800000, v36
	v_mul_f32_e32 v107, 0x43800000, v37
	v_cvt_pk_fp8_f32 v126, v67, v105
	v_cvt_pk_fp8_f32 v117, v106, v107 op_sel:[0,0,1]
	v_mul_f32_e32 v106, 0x43800000, v44
	v_mul_f32_e32 v107, 0x43800000, v45
	v_cvt_pk_fp8_f32 v121, v106, v107 op_sel:[0,0,1]
	v_mul_f32_e32 v106, 0x43800000, v52
	v_mul_f32_e32 v107, 0x43800000, v53
	v_cvt_pk_fp8_f32 v123, v106, v107 op_sel:[0,0,1]
	v_mul_f32_e32 v106, 0x43800000, v60
	v_mul_f32_e32 v107, 0x43800000, v61
	v_mul_f32_e32 v67, 0x43800000, v64
	v_mul_f32_e32 v105, 0x43800000, v65
	v_cvt_pk_fp8_f32 v125, v106, v107 op_sel:[0,0,1]
	v_cvt_pk_fp8_f32 v126, v67, v105 op_sel:[0,0,1]
	s_mov_b32 s0, 0x5010400
	s_mov_b32 s1, 0x7030602
	v_perm_b32 v67, v109, v108, s0
	v_perm_b32 v105, v109, v108, s1
	v_perm_b32 v107, v111, v110, s0
	v_perm_b32 v108, v111, v110, s1
	s_mov_b32 s4, 0x5040100
	s_mov_b32 s3, 0x7060302
	v_perm_b32 v106, v107, v67, s4
	v_perm_b32 v110, v107, v67, s3
	v_perm_b32 v114, v108, v105, s4
	v_perm_b32 v118, v108, v105, s3
	v_perm_b32 v67, v113, v112, s0
	v_perm_b32 v105, v113, v112, s1
	v_perm_b32 v108, v116, v115, s0
	v_perm_b32 v109, v116, v115, s1
	v_perm_b32 v107, v108, v67, s4
	v_perm_b32 v111, v108, v67, s3
	v_perm_b32 v115, v109, v105, s4
	v_perm_b32 v119, v109, v105, s3
	v_perm_b32 v67, v120, v117, s0
	v_perm_b32 v105, v120, v117, s1
	v_perm_b32 v109, v122, v121, s0
	v_perm_b32 v113, v122, v121, s1
	v_perm_b32 v108, v109, v67, s4
	v_perm_b32 v112, v109, v67, s3
	v_perm_b32 v116, v113, v105, s4
	v_perm_b32 v120, v113, v105, s3
	v_perm_b32 v67, v124, v123, s0
	v_perm_b32 v113, v126, v125, s0
	v_perm_b32 v105, v124, v123, s1
	v_perm_b32 v121, v126, v125, s1
	v_perm_b32 v109, v113, v67, s4
	v_perm_b32 v113, v113, v67, s3
	v_add_u32_e32 v67, s22, v130
	v_perm_b32 v117, v121, v105, s4
	v_perm_b32 v121, v121, v105, s3
	ds_write_b128 v67, v[106:109]
	ds_write_b128 v67, v[110:113] offset:128
	ds_write_b128 v67, v[114:117] offset:256
	ds_write_b128 v67, v[118:121] offset:384
	s_waitcnt lgkmcnt(0)
	s_waitcnt lgkmcnt(0)
	s_barrier
	s_cbranch_execz .Lpb1_496

; #define GAS __attribute__((address_space(1)))
; #define LAS __attribute__((address_space(3)))
; __device__ __forceinline__ void cv8_out(const CvTile& cur, const LAS unsigned char* T, int tid_) {
;     const int nbl = cur.N / 256, kb = cur.r / nbl, nb = cur.r - kb * nbl;
; #pragma unroll
;     for (int i = 0; i < 4; ++i) { const int p = tid_ + 512 * i, c = p & 7, n = p >> 3, nn = 256 * nb + n;
;         const int drow = (cur.mode == 0) ? nn : (256 * (nn >> 7) + (nn & 127) + (cur.mode == 2 ? 128 : 0));
;         const v4u w = *(const LAS v4u*)(T + n * 128 + 16 * (c ^ ((n >> 2) & 7)));
;         __builtin_nontemporal_store(w, (GAS v4u*)(cur.WT + (size_t)drow * cur.K + 128 * kb + 16 * c)); }
; }
.Lpb1_494:
	s_waitcnt vmcnt(31)
	v_add_u32_e32 v2, s64, v102
	v_lshlrev_b32_e32 v3, 1, v2
	v_and_b32_e32 v3, 0xffffff00, v3
	v_or3_b32 v3, v100, v3, s18
	s_waitcnt vmcnt(29)
	v_add_u32_e32 v10, s22, v101
	v_cndmask_b32_e64 v8, v3, v2, s[62:63]
	v_add_u32_e32 v2, v10, v99
	v_ashrrev_i32_e32 v6, 31, v8
	ds_read_b128 v[2:5], v2
	v_mul_lo_u32 v11, s60, v6
	v_mov_b64_e32 v[6:7], s[58:59]
	v_mul_lo_u32 v12, s61, v8
	v_mad_u64_u32 v[8:9], s[0:1], s60, v8, v[6:7]
	s_ashr_i32 s71, s70, 31
	v_add3_u32 v9, v12, v9, v11
	v_lshl_add_u64 v[8:9], v[8:9], 0, s[70:71]
	v_lshl_add_u64 v[8:9], v[8:9], 0, v[0:1]
	s_waitcnt lgkmcnt(0)
	global_store_dwordx4 v[8:9], v[2:5], off nt
	s_nop 1
	v_add_u32_e32 v2, s64, v98
	v_lshlrev_b32_e32 v3, 1, v2
	v_and_b32_e32 v3, 0xffffff00, v3
	v_or3_b32 v3, v97, v3, s18
	v_cndmask_b32_e64 v8, v3, v2, s[62:63]
	v_add_u32_e32 v2, v10, v96
	ds_read_b128 v[2:5], v2
	v_ashrrev_i32_e32 v9, 31, v8
	v_mul_lo_u32 v11, s60, v9
	v_mul_lo_u32 v12, s61, v8
	v_mad_u64_u32 v[8:9], s[0:1], s60, v8, v[6:7]
	v_add3_u32 v9, v12, v9, v11
	v_lshl_add_u64 v[8:9], v[8:9], 0, s[70:71]
	v_lshl_add_u64 v[8:9], v[8:9], 0, v[0:1]
	s_waitcnt lgkmcnt(0)
	global_store_dwordx4 v[8:9], v[2:5], off nt
	s_nop 1
	v_add_u32_e32 v2, s64, v94
	v_lshlrev_b32_e32 v3, 1, v2
	v_and_b32_e32 v3, 0xffffff00, v3
	v_or3_b32 v3, v93, v3, s18
	v_cndmask_b32_e64 v8, v3, v2, s[62:63]
	v_add_u32_e32 v2, v10, v92
	ds_read_b128 v[2:5], v2
	v_ashrrev_i32_e32 v9, 31, v8
	v_mul_lo_u32 v11, s60, v9
	v_mul_lo_u32 v12, s61, v8
	v_mad_u64_u32 v[8:9], s[0:1], s60, v8, v[6:7]
	v_add3_u32 v9, v12, v9, v11
	v_lshl_add_u64 v[8:9], v[8:9], 0, s[70:71]
	v_lshl_add_u64 v[8:9], v[8:9], 0, v[0:1]
	s_waitcnt lgkmcnt(0)
	global_store_dwordx4 v[8:9], v[2:5], off nt
	s_nop 1
	v_add_u32_e32 v2, s64, v91
	v_lshlrev_b32_e32 v3, 1, v2
	v_and_b32_e32 v3, 0xffffff00, v3
	v_or3_b32 v3, v90, v3, s18
	v_cndmask_b32_e64 v8, v3, v2, s[62:63]
	v_add_u32_e32 v2, v10, v89
	ds_read_b128 v[2:5], v2
	v_ashrrev_i32_e32 v9, 31, v8
	v_mul_lo_u32 v9, s60, v9
	v_mul_lo_u32 v10, s61, v8
	v_mad_u64_u32 v[6:7], s[0:1], s60, v8, v[6:7]
	v_add3_u32 v7, v10, v7, v9
	v_lshl_add_u64 v[6:7], v[6:7], 0, s[70:71]
	v_lshl_add_u64 v[6:7], v[6:7], 0, v[0:1]
	s_waitcnt lgkmcnt(0)
	global_store_dwordx4 v[6:7], v[2:5], off nt
	s_waitcnt lgkmcnt(0)
	s_barrier
	s_cbranch_execz .Lpb1_498
	s_branch .Lpipe_b1_done

.Lpb1_496:
	s_waitcnt vmcnt(31)
	ds_write_b128 v131, v[2:5]
	s_waitcnt vmcnt(30)
	ds_write_b128 v131, v[6:9] offset:1040
	s_waitcnt vmcnt(29)
	ds_write_b128 v131, v[10:13] offset:2080
	s_waitcnt vmcnt(28)
	ds_write_b128 v131, v[14:17] offset:3120
	s_waitcnt vmcnt(27)
	ds_write_b128 v131, v[18:21] offset:4160
	s_waitcnt vmcnt(26)
	ds_write_b128 v131, v[22:25] offset:5200
	s_waitcnt vmcnt(25)
	ds_write_b128 v131, v[26:29] offset:6240
	s_waitcnt vmcnt(24)
	ds_write_b128 v131, v[30:33] offset:7280
	s_waitcnt vmcnt(23)
	ds_write_b128 v131, v[34:37] offset:8320
	s_waitcnt vmcnt(22)
	ds_write_b128 v131, v[38:41] offset:9360
	s_waitcnt vmcnt(21)
	ds_write_b128 v131, v[42:45] offset:10400
	s_waitcnt vmcnt(20)
	ds_write_b128 v131, v[46:49] offset:11440
	s_waitcnt vmcnt(19)
	ds_write_b128 v131, v[50:53] offset:12480
	s_waitcnt vmcnt(18)
	ds_write_b128 v131, v[54:57] offset:13520
	s_waitcnt vmcnt(17)
	ds_write_b128 v131, v[58:61] offset:14560
	s_waitcnt vmcnt(16)
	ds_write_b128 v131, v[62:65] offset:15600
	s_waitcnt lgkmcnt(0)
	s_waitcnt lgkmcnt(0)
	s_barrier
	s_andn2_b64 vcc, exec, s[28:29]
	s_mov_b64 s[0:1], -1
	s_cbranch_vccz .Lpb1_494

; #define GAS __attribute__((address_space(1)))
; #define LAS __attribute__((address_space(3)))
; __device__ __forceinline__ unsigned pk2(float lo, float hi) { return f2bf(lo) | (f2bf(hi) << 16); }
; __device__ __forceinline__ void cv_tile_out(const CvTile& cur, LAS float* S, int tid_) {
;     ...
; #pragma unroll
;         for (int i = 0; i < 8; ++i) { const int p = tid_ + 512 * i, kc = p & 15, n = p >> 4, nn = 256 * nb + n;
;             const int drow = (cur.mode == 0) ? nn : (256 * (nn >> 7) + (nn & 127) + (cur.mode == 2 ? 128 : 0));
;             const LAS float* sp = S + (8 * kc) * LS + (n ^ (4 * (kc >> 1))); v4u o;
;             o.x = pk2(sp[0], sp[LS]); o.y = pk2(sp[2 * LS], sp[3 * LS]); o.z = pk2(sp[4 * LS], sp[5 * LS]); o.w = pk2(sp[6 * LS], sp[7 * LS]);
;             *(GAS v4u*)((bf16*)cur.WT + (size_t)drow * cur.K + 128 * kb + 8 * kc) = o; } }
.Lpb1_498:
	v_add_u32_e32 v0, s64, v104
	s_waitcnt vmcnt(31)
	v_lshlrev_b32_e32 v2, 1, v0
	v_and_b32_e32 v2, 0xffffff00, v2
	v_or3_b32 v2, v103, v2, s18
	v_cndmask_b32_e64 v0, v2, v0, s[62:63]
	ds_read_b32 v2, v95
	ds_read_b32 v3, v95 offset:1040
	s_waitcnt vmcnt(30)
	v_mul_lo_u32 v9, s61, v0
	s_ashr_i32 s71, s70, 31
	s_lshl_b64 s[28:29], s[70:71], 1
	s_waitcnt lgkmcnt(1)
	v_bfe_u32 v4, v2, 16, 1
	v_add3_u32 v2, v2, v4, s10
	s_waitcnt lgkmcnt(0)
	v_bfe_u32 v4, v3, 16, 1
	v_lshrrev_b32_e32 v2, 16, v2
	v_add3_u32 v3, v3, v4, s10
	v_and_or_b32 v2, v3, s11, v2
	ds_read_b32 v3, v95 offset:2080
	ds_read_b32 v4, v95 offset:3120
	v_mov_b32_e32 v67, v1
	s_waitcnt lgkmcnt(1)
	v_bfe_u32 v5, v3, 16, 1
	v_add3_u32 v3, v3, v5, s10
	s_waitcnt lgkmcnt(0)
	v_bfe_u32 v5, v4, 16, 1
	v_lshrrev_b32_e32 v3, 16, v3
	v_add3_u32 v4, v4, v5, s10
	v_and_or_b32 v3, v4, s11, v3
	ds_read_b32 v4, v95 offset:4160
	ds_read_b32 v5, v95 offset:5200
	s_waitcnt lgkmcnt(1)
	v_bfe_u32 v6, v4, 16, 1
	v_add3_u32 v4, v4, v6, s10
	s_waitcnt lgkmcnt(0)
	v_bfe_u32 v6, v5, 16, 1
	v_lshrrev_b32_e32 v4, 16, v4
	v_add3_u32 v5, v5, v6, s10
	v_and_or_b32 v4, v5, s11, v4
	ds_read_b32 v5, v95 offset:6240
	ds_read_b32 v6, v95 offset:7280
	s_waitcnt lgkmcnt(1)
	v_bfe_u32 v7, v5, 16, 1
	v_add3_u32 v5, v5, v7, s10
	s_waitcnt lgkmcnt(0)
	v_bfe_u32 v7, v6, 16, 1
	v_lshrrev_b32_e32 v5, 16, v5
	v_add3_u32 v6, v6, v7, s10
	v_and_or_b32 v5, v6, s11, v5
	v_ashrrev_i32_e32 v6, 31, v0
	v_mul_lo_u32 v8, s60, v6
	v_mad_u64_u32 v[6:7], s[0:1], s60, v0, 0
	v_add3_u32 v7, v7, v8, v9
	v_lshl_add_u64 v[6:7], v[6:7], 1, s[58:59]
	v_lshl_add_u64 v[6:7], v[6:7], 0, s[28:29]
	v_lshl_add_u64 v[6:7], v[6:7], 0, v[66:67]
	v_add_u32_e32 v0, s64, v88
	global_store_dwordx4 v[6:7], v[2:5], off
	s_nop 1
	v_lshlrev_b32_e32 v2, 1, v0
	v_and_b32_e32 v2, 0xffffff00, v2
	v_or3_b32 v2, v87, v2, s18
	v_cndmask_b32_e64 v0, v2, v0, s[62:63]
	ds_read_b32 v2, v86
	ds_read_b32 v3, v86 offset:1040
	v_mul_lo_u32 v9, s61, v0
	s_waitcnt lgkmcnt(1)
	v_bfe_u32 v4, v2, 16, 1
	v_add3_u32 v2, v2, v4, s10
	s_waitcnt lgkmcnt(0)
	v_bfe_u32 v4, v3, 16, 1
	v_lshrrev_b32_e32 v2, 16, v2
	v_add3_u32 v3, v3, v4, s10
	v_and_or_b32 v2, v3, s11, v2
	ds_read_b32 v3, v86 offset:2080
	ds_read_b32 v4, v86 offset:3120
	s_waitcnt lgkmcnt(1)
	v_bfe_u32 v5, v3, 16, 1
	v_add3_u32 v3, v3, v5, s10
	s_waitcnt lgkmcnt(0)
	v_bfe_u32 v5, v4, 16, 1
	v_lshrrev_b32_e32 v3, 16, v3
	v_add3_u32 v4, v4, v5, s10
	v_and_or_b32 v3, v4, s11, v3
	ds_read_b32 v4, v86 offset:4160
	ds_read_b32 v5, v86 offset:5200
	s_waitcnt lgkmcnt(1)
	v_bfe_u32 v6, v4, 16, 1
	v_add3_u32 v4, v4, v6, s10
	s_waitcnt lgkmcnt(0)
	v_bfe_u32 v6, v5, 16, 1
	v_lshrrev_b32_e32 v4, 16, v4
	v_add3_u32 v5, v5, v6, s10
	v_and_or_b32 v4, v5, s11, v4
	ds_read_b32 v5, v86 offset:6240
	ds_read_b32 v6, v86 offset:7280
	s_waitcnt lgkmcnt(1)
	v_bfe_u32 v7, v5, 16, 1
	v_add3_u32 v5, v5, v7, s10
	s_waitcnt lgkmcnt(0)
	v_bfe_u32 v7, v6, 16, 1
	v_lshrrev_b32_e32 v5, 16, v5
	v_add3_u32 v6, v6, v7, s10
	v_and_or_b32 v5, v6, s11, v5
	v_ashrrev_i32_e32 v6, 31, v0
	v_mul_lo_u32 v8, s60, v6
	v_mad_u64_u32 v[6:7], s[0:1], s60, v0, 0
	v_add3_u32 v7, v7, v8, v9
	v_lshl_add_u64 v[6:7], v[6:7], 1, s[58:59]
	v_lshl_add_u64 v[6:7], v[6:7], 0, s[28:29]
	v_lshl_add_u64 v[6:7], v[6:7], 0, v[66:67]
	v_add_u32_e32 v0, s64, v85
	global_store_dwordx4 v[6:7], v[2:5], off
	s_nop 1
	v_lshlrev_b32_e32 v2, 1, v0
	v_and_b32_e32 v2, 0xffffff00, v2
	v_or3_b32 v2, v84, v2, s18
	v_cndmask_b32_e64 v0, v2, v0, s[62:63]
	ds_read_b32 v2, v83
	ds_read_b32 v3, v83 offset:1040
	v_mul_lo_u32 v9, s61, v0
	s_waitcnt lgkmcnt(1)
	v_bfe_u32 v4, v2, 16, 1
	v_add3_u32 v2, v2, v4, s10
	s_waitcnt lgkmcnt(0)
	v_bfe_u32 v4, v3, 16, 1
	v_lshrrev_b32_e32 v2, 16, v2
	v_add3_u32 v3, v3, v4, s10
	v_and_or_b32 v2, v3, s11, v2
	ds_read_b32 v3, v83 offset:2080
	ds_read_b32 v4, v83 offset:3120
	s_waitcnt lgkmcnt(1)
	v_bfe_u32 v5, v3, 16, 1
	v_add3_u32 v3, v3, v5, s10
	s_waitcnt lgkmcnt(0)
	v_bfe_u32 v5, v4, 16, 1
	v_lshrrev_b32_e32 v3, 16, v3
	v_add3_u32 v4, v4, v5, s10
	v_and_or_b32 v3, v4, s11, v3
	ds_read_b32 v4, v83 offset:4160
	ds_read_b32 v5, v83 offset:5200
	s_waitcnt lgkmcnt(1)
	v_bfe_u32 v6, v4, 16, 1
	v_add3_u32 v4, v4, v6, s10
	s_waitcnt lgkmcnt(0)
	v_bfe_u32 v6, v5, 16, 1
	v_lshrrev_b32_e32 v4, 16, v4
	v_add3_u32 v5, v5, v6, s10
	v_and_or_b32 v4, v5, s11, v4
	ds_read_b32 v5, v83 offset:6240
	ds_read_b32 v6, v83 offset:7280
	s_waitcnt lgkmcnt(1)
	v_bfe_u32 v7, v5, 16, 1
	v_add3_u32 v5, v5, v7, s10
	s_waitcnt lgkmcnt(0)
	v_bfe_u32 v7, v6, 16, 1
	v_lshrrev_b32_e32 v5, 16, v5
	v_add3_u32 v6, v6, v7, s10
	v_and_or_b32 v5, v6, s11, v5
	v_ashrrev_i32_e32 v6, 31, v0
	v_mul_lo_u32 v8, s60, v6
	v_mad_u64_u32 v[6:7], s[0:1], s60, v0, 0
	v_add3_u32 v7, v7, v8, v9
	v_lshl_add_u64 v[6:7], v[6:7], 1, s[58:59]
	v_lshl_add_u64 v[6:7], v[6:7], 0, s[28:29]
	v_lshl_add_u64 v[6:7], v[6:7], 0, v[66:67]
	v_add_u32_e32 v0, s64, v82
	global_store_dwordx4 v[6:7], v[2:5], off
	s_nop 1
	v_lshlrev_b32_e32 v2, 1, v0
	v_and_b32_e32 v2, 0xffffff00, v2
	v_or3_b32 v2, v81, v2, s18
	v_cndmask_b32_e64 v0, v2, v0, s[62:63]
	ds_read_b32 v2, v80
	ds_read_b32 v3, v80 offset:1040
	v_mul_lo_u32 v9, s61, v0
	s_waitcnt lgkmcnt(1)
	v_bfe_u32 v4, v2, 16, 1
	v_add3_u32 v2, v2, v4, s10
	s_waitcnt lgkmcnt(0)
	v_bfe_u32 v4, v3, 16, 1
	v_lshrrev_b32_e32 v2, 16, v2
	v_add3_u32 v3, v3, v4, s10
	v_and_or_b32 v2, v3, s11, v2
	ds_read_b32 v3, v80 offset:2080
	ds_read_b32 v4, v80 offset:3120
	s_waitcnt lgkmcnt(1)
	v_bfe_u32 v5, v3, 16, 1
	v_add3_u32 v3, v3, v5, s10
	s_waitcnt lgkmcnt(0)
	v_bfe_u32 v5, v4, 16, 1
	v_lshrrev_b32_e32 v3, 16, v3
	v_add3_u32 v4, v4, v5, s10
	v_and_or_b32 v3, v4, s11, v3
	ds_read_b32 v4, v80 offset:4160
	ds_read_b32 v5, v80 offset:5200
	s_waitcnt lgkmcnt(1)
; #define GAS __attribute__((address_space(1)))
; #define LAS __attribute__((address_space(3)))
; __device__ __forceinline__ unsigned pk2(float lo, float hi) { return f2bf(lo) | (f2bf(hi) << 16); }
; __device__ __forceinline__ void cv_tile_out(const CvTile& cur, LAS float* S, int tid_) {
;     ...
; #pragma unroll
;         for (int i = 0; i < 8; ++i) { const int p = tid_ + 512 * i, kc = p & 15, n = p >> 4, nn = 256 * nb + n;
;             const int drow = (cur.mode == 0) ? nn : (256 * (nn >> 7) + (nn & 127) + (cur.mode == 2 ? 128 : 0));
;             const LAS float* sp = S + (8 * kc) * LS + (n ^ (4 * (kc >> 1))); v4u o;
;             o.x = pk2(sp[0], sp[LS]); o.y = pk2(sp[2 * LS], sp[3 * LS]); o.z = pk2(sp[4 * LS], sp[5 * LS]); o.w = pk2(sp[6 * LS], sp[7 * LS]);
;             *(GAS v4u*)((bf16*)cur.WT + (size_t)drow * cur.K + 128 * kb + 8 * kc) = o; } }
	v_bfe_u32 v6, v4, 16, 1
	v_add3_u32 v4, v4, v6, s10
	s_waitcnt lgkmcnt(0)
	v_bfe_u32 v6, v5, 16, 1
	v_lshrrev_b32_e32 v4, 16, v4
	v_add3_u32 v5, v5, v6, s10
	v_and_or_b32 v4, v5, s11, v4
	ds_read_b32 v5, v80 offset:6240
	ds_read_b32 v6, v80 offset:7280
	s_waitcnt lgkmcnt(1)
	v_bfe_u32 v7, v5, 16, 1
	v_add3_u32 v5, v5, v7, s10
	s_waitcnt lgkmcnt(0)
	v_bfe_u32 v7, v6, 16, 1
	v_lshrrev_b32_e32 v5, 16, v5
	v_add3_u32 v6, v6, v7, s10
	v_and_or_b32 v5, v6, s11, v5
	v_ashrrev_i32_e32 v6, 31, v0
	v_mul_lo_u32 v8, s60, v6
	v_mad_u64_u32 v[6:7], s[0:1], s60, v0, 0
	v_add3_u32 v7, v7, v8, v9
	v_lshl_add_u64 v[6:7], v[6:7], 1, s[58:59]
	v_lshl_add_u64 v[6:7], v[6:7], 0, s[28:29]
	v_lshl_add_u64 v[6:7], v[6:7], 0, v[66:67]
	v_add_u32_e32 v0, s64, v79
	global_store_dwordx4 v[6:7], v[2:5], off
	s_nop 1
	v_lshlrev_b32_e32 v2, 1, v0
	v_and_b32_e32 v2, 0xffffff00, v2
	v_or3_b32 v2, v78, v2, s18
	v_cndmask_b32_e64 v0, v2, v0, s[62:63]
	ds_read_b32 v2, v77
	ds_read_b32 v3, v77 offset:1040
	v_mul_lo_u32 v9, s61, v0
	s_waitcnt lgkmcnt(1)
	v_bfe_u32 v4, v2, 16, 1
	v_add3_u32 v2, v2, v4, s10
	s_waitcnt lgkmcnt(0)
	v_bfe_u32 v4, v3, 16, 1
	v_lshrrev_b32_e32 v2, 16, v2
	v_add3_u32 v3, v3, v4, s10
	v_and_or_b32 v2, v3, s11, v2
	ds_read_b32 v3, v77 offset:2080
	ds_read_b32 v4, v77 offset:3120
	s_waitcnt lgkmcnt(1)
	v_bfe_u32 v5, v3, 16, 1
	v_add3_u32 v3, v3, v5, s10
	s_waitcnt lgkmcnt(0)
	v_bfe_u32 v5, v4, 16, 1
	v_lshrrev_b32_e32 v3, 16, v3
	v_add3_u32 v4, v4, v5, s10
	v_and_or_b32 v3, v4, s11, v3
	ds_read_b32 v4, v77 offset:4160
	ds_read_b32 v5, v77 offset:5200
	s_waitcnt lgkmcnt(1)
	v_bfe_u32 v6, v4, 16, 1
	v_add3_u32 v4, v4, v6, s10
	s_waitcnt lgkmcnt(0)
	v_bfe_u32 v6, v5, 16, 1
	v_lshrrev_b32_e32 v4, 16, v4
	v_add3_u32 v5, v5, v6, s10
	v_and_or_b32 v4, v5, s11, v4
	ds_read_b32 v5, v77 offset:6240
	ds_read_b32 v6, v77 offset:7280
	s_waitcnt lgkmcnt(1)
	v_bfe_u32 v7, v5, 16, 1
	v_add3_u32 v5, v5, v7, s10
	s_waitcnt lgkmcnt(0)
	v_bfe_u32 v7, v6, 16, 1
	v_lshrrev_b32_e32 v5, 16, v5
	v_add3_u32 v6, v6, v7, s10
	v_and_or_b32 v5, v6, s11, v5
	v_ashrrev_i32_e32 v6, 31, v0
	v_mul_lo_u32 v8, s60, v6
	v_mad_u64_u32 v[6:7], s[0:1], s60, v0, 0
	v_add3_u32 v7, v7, v8, v9
	v_lshl_add_u64 v[6:7], v[6:7], 1, s[58:59]
	v_lshl_add_u64 v[6:7], v[6:7], 0, s[28:29]
	v_lshl_add_u64 v[6:7], v[6:7], 0, v[66:67]
	v_add_u32_e32 v0, s64, v76
	global_store_dwordx4 v[6:7], v[2:5], off
	s_nop 1
	v_lshlrev_b32_e32 v2, 1, v0
	v_and_b32_e32 v2, 0xffffff00, v2
	v_or3_b32 v2, v75, v2, s18
	v_cndmask_b32_e64 v0, v2, v0, s[62:63]
	ds_read_b32 v2, v74
	ds_read_b32 v3, v74 offset:1040
	v_mul_lo_u32 v9, s61, v0
	s_waitcnt lgkmcnt(1)
	v_bfe_u32 v4, v2, 16, 1
	v_add3_u32 v2, v2, v4, s10
	s_waitcnt lgkmcnt(0)
	v_bfe_u32 v4, v3, 16, 1
	v_lshrrev_b32_e32 v2, 16, v2
	v_add3_u32 v3, v3, v4, s10
	v_and_or_b32 v2, v3, s11, v2
	ds_read_b32 v3, v74 offset:2080
	ds_read_b32 v4, v74 offset:3120
	s_waitcnt lgkmcnt(1)
	v_bfe_u32 v5, v3, 16, 1
	v_add3_u32 v3, v3, v5, s10
	s_waitcnt lgkmcnt(0)
	v_bfe_u32 v5, v4, 16, 1
	v_lshrrev_b32_e32 v3, 16, v3
	v_add3_u32 v4, v4, v5, s10
	v_and_or_b32 v3, v4, s11, v3
	ds_read_b32 v4, v74 offset:4160
	ds_read_b32 v5, v74 offset:5200
	s_waitcnt lgkmcnt(1)
	v_bfe_u32 v6, v4, 16, 1
	v_add3_u32 v4, v4, v6, s10
	s_waitcnt lgkmcnt(0)
	v_bfe_u32 v6, v5, 16, 1
	v_lshrrev_b32_e32 v4, 16, v4
	v_add3_u32 v5, v5, v6, s10
	v_and_or_b32 v4, v5, s11, v4
	ds_read_b32 v5, v74 offset:6240
	ds_read_b32 v6, v74 offset:7280
	s_waitcnt lgkmcnt(1)
	v_bfe_u32 v7, v5, 16, 1
	v_add3_u32 v5, v5, v7, s10
	s_waitcnt lgkmcnt(0)
	v_bfe_u32 v7, v6, 16, 1
	v_lshrrev_b32_e32 v5, 16, v5
	v_add3_u32 v6, v6, v7, s10
	v_and_or_b32 v5, v6, s11, v5
	v_ashrrev_i32_e32 v6, 31, v0
	v_mul_lo_u32 v8, s60, v6
	v_mad_u64_u32 v[6:7], s[0:1], s60, v0, 0
	v_add3_u32 v7, v7, v8, v9
	v_lshl_add_u64 v[6:7], v[6:7], 1, s[58:59]
	v_lshl_add_u64 v[6:7], v[6:7], 0, s[28:29]
	v_lshl_add_u64 v[6:7], v[6:7], 0, v[66:67]
	v_add_u32_e32 v0, s64, v73
	global_store_dwordx4 v[6:7], v[2:5], off
	s_nop 1
	v_lshlrev_b32_e32 v2, 1, v0
	v_and_b32_e32 v2, 0xffffff00, v2
	v_or3_b32 v2, v72, v2, s18
	v_cndmask_b32_e64 v0, v2, v0, s[62:63]
	ds_read_b32 v2, v71
	ds_read_b32 v3, v71 offset:1040
	v_mul_lo_u32 v9, s61, v0
	s_waitcnt lgkmcnt(1)
	v_bfe_u32 v4, v2, 16, 1
	v_add3_u32 v2, v2, v4, s10
	s_waitcnt lgkmcnt(0)
	v_bfe_u32 v4, v3, 16, 1
	v_lshrrev_b32_e32 v2, 16, v2
	v_add3_u32 v3, v3, v4, s10
	v_and_or_b32 v2, v3, s11, v2
	ds_read_b32 v3, v71 offset:2080
	ds_read_b32 v4, v71 offset:3120
	s_waitcnt lgkmcnt(1)
; #define GAS __attribute__((address_space(1)))
; #define LAS __attribute__((address_space(3)))
; __device__ __forceinline__ unsigned pk2(float lo, float hi) { return f2bf(lo) | (f2bf(hi) << 16); }
; __device__ __forceinline__ void cv_tile_out(const CvTile& cur, LAS float* S, int tid_) {
;     ...
; #pragma unroll
;         for (int i = 0; i < 8; ++i) { const int p = tid_ + 512 * i, kc = p & 15, n = p >> 4, nn = 256 * nb + n;
;             const int drow = (cur.mode == 0) ? nn : (256 * (nn >> 7) + (nn & 127) + (cur.mode == 2 ? 128 : 0));
;             const LAS float* sp = S + (8 * kc) * LS + (n ^ (4 * (kc >> 1))); v4u o;
;             o.x = pk2(sp[0], sp[LS]); o.y = pk2(sp[2 * LS], sp[3 * LS]); o.z = pk2(sp[4 * LS], sp[5 * LS]); o.w = pk2(sp[6 * LS], sp[7 * LS]);
;             *(GAS v4u*)((bf16*)cur.WT + (size_t)drow * cur.K + 128 * kb + 8 * kc) = o; } }
	v_bfe_u32 v5, v3, 16, 1
	v_add3_u32 v3, v3, v5, s10
	s_waitcnt lgkmcnt(0)
	v_bfe_u32 v5, v4, 16, 1
	v_lshrrev_b32_e32 v3, 16, v3
	v_add3_u32 v4, v4, v5, s10
	v_and_or_b32 v3, v4, s11, v3
	ds_read_b32 v4, v71 offset:4160
	ds_read_b32 v5, v71 offset:5200
	s_waitcnt lgkmcnt(1)
	v_bfe_u32 v6, v4, 16, 1
	v_add3_u32 v4, v4, v6, s10
	s_waitcnt lgkmcnt(0)
	v_bfe_u32 v6, v5, 16, 1
	v_lshrrev_b32_e32 v4, 16, v4
	v_add3_u32 v5, v5, v6, s10
	v_and_or_b32 v4, v5, s11, v4
	ds_read_b32 v5, v71 offset:6240
	ds_read_b32 v6, v71 offset:7280
	s_waitcnt lgkmcnt(1)
	v_bfe_u32 v7, v5, 16, 1
	v_add3_u32 v5, v5, v7, s10
	s_waitcnt lgkmcnt(0)
	v_bfe_u32 v7, v6, 16, 1
	v_lshrrev_b32_e32 v5, 16, v5
	v_add3_u32 v6, v6, v7, s10
	v_and_or_b32 v5, v6, s11, v5
	v_ashrrev_i32_e32 v6, 31, v0
	v_mul_lo_u32 v8, s60, v6
	v_mad_u64_u32 v[6:7], s[0:1], s60, v0, 0
	v_add3_u32 v7, v7, v8, v9
	v_lshl_add_u64 v[6:7], v[6:7], 1, s[58:59]
	v_lshl_add_u64 v[6:7], v[6:7], 0, s[28:29]
	v_lshl_add_u64 v[6:7], v[6:7], 0, v[66:67]
	v_add_u32_e32 v0, s64, v70
	global_store_dwordx4 v[6:7], v[2:5], off
	s_nop 1
	v_lshlrev_b32_e32 v2, 1, v0
	v_and_b32_e32 v2, 0xffffff00, v2
	v_or3_b32 v2, v69, v2, s18
	v_cndmask_b32_e64 v0, v2, v0, s[62:63]
	ds_read_b32 v2, v68
	ds_read_b32 v3, v68 offset:1040
	v_mul_lo_u32 v9, s61, v0
	s_waitcnt lgkmcnt(1)
	v_bfe_u32 v4, v2, 16, 1
	v_add3_u32 v2, v2, v4, s10
	s_waitcnt lgkmcnt(0)
	v_bfe_u32 v4, v3, 16, 1
	v_lshrrev_b32_e32 v2, 16, v2
	v_add3_u32 v3, v3, v4, s10
	v_and_or_b32 v2, v3, s11, v2
	ds_read_b32 v3, v68 offset:2080
	ds_read_b32 v4, v68 offset:3120
	s_waitcnt lgkmcnt(1)
	v_bfe_u32 v5, v3, 16, 1
	v_add3_u32 v3, v3, v5, s10
	s_waitcnt lgkmcnt(0)
	v_bfe_u32 v5, v4, 16, 1
	v_lshrrev_b32_e32 v3, 16, v3
	v_add3_u32 v4, v4, v5, s10
	v_and_or_b32 v3, v4, s11, v3
	ds_read_b32 v4, v68 offset:4160
	ds_read_b32 v5, v68 offset:5200
	s_waitcnt lgkmcnt(1)
	v_bfe_u32 v6, v4, 16, 1
	v_add3_u32 v4, v4, v6, s10
	s_waitcnt lgkmcnt(0)
	v_bfe_u32 v6, v5, 16, 1
	v_lshrrev_b32_e32 v4, 16, v4
	v_add3_u32 v5, v5, v6, s10
	v_and_or_b32 v4, v5, s11, v4
	ds_read_b32 v5, v68 offset:6240
	ds_read_b32 v6, v68 offset:7280
	s_waitcnt lgkmcnt(1)
	v_bfe_u32 v7, v5, 16, 1
	v_add3_u32 v5, v5, v7, s10
	s_waitcnt lgkmcnt(0)
	v_bfe_u32 v7, v6, 16, 1
	v_lshrrev_b32_e32 v5, 16, v5
	v_add3_u32 v6, v6, v7, s10
	v_and_or_b32 v5, v6, s11, v5
	v_ashrrev_i32_e32 v6, 31, v0
	v_mul_lo_u32 v8, s60, v6
	v_mad_u64_u32 v[6:7], s[0:1], s60, v0, 0
	v_add3_u32 v7, v7, v8, v9
	v_lshl_add_u64 v[6:7], v[6:7], 1, s[58:59]
	v_lshl_add_u64 v[6:7], v[6:7], 0, s[28:29]
	v_lshl_add_u64 v[6:7], v[6:7], 0, v[66:67]
	global_store_dwordx4 v[6:7], v[2:5], off
	s_waitcnt lgkmcnt(0)
	s_barrier
.Lpipe_b1_done:
	v_readlane_b32 s0, v151, 0
	v_readlane_b32 s1, v151, 1
	v_readlane_b32 s2, v151, 2
	v_readlane_b32 s14, v151, 3
	v_readlane_b32 s16, v151, 4
	v_readlane_b32 s17, v151, 5
	v_readlane_b32 s18, v151, 6
	v_readlane_b32 s19, v151, 7
	v_readlane_b32 s22, v151, 8
	v_readlane_b32 s23, v151, 9
	v_readlane_b32 s27, v151, 10
	v_readlane_b32 s28, v151, 11
	v_readlane_b32 s29, v151, 12
	v_readlane_b32 s30, v151, 13
	v_readlane_b32 s40, v151, 14
	v_readlane_b32 s41, v151, 15
	v_readlane_b32 s42, v151, 16
	v_readlane_b32 s43, v151, 17
	v_readlane_b32 s44, v151, 18
	v_readlane_b32 s45, v151, 19
	v_readlane_b32 s46, v151, 20
	v_readlane_b32 s47, v151, 21
	v_readlane_b32 s56, v151, 22
	v_readlane_b32 s66, v151, 23
	v_readlane_b32 s67, v151, 24
	v_readlane_b32 s68, v151, 25
	v_readlane_b32 s69, v151, 26
	v_readlane_b32 s72, v151, 27
	v_readlane_b32 s73, v151, 28
	v_readlane_b32 s76, v151, 29
	v_readlane_b32 s77, v151, 30
	v_readlane_b32 s84, v151, 31
	v_readlane_b32 s85, v151, 32
	s_nop 4
	v_mov_b32_e32 v2, v136
	v_mov_b32_e32 v3, v137
	s_and_b64 vcc, exec, s[42:43]
	s_cbranch_vccz .Lpd_473
	s_cmpk_gt_u32 s15, 0xff
	s_mov_b64 s[0:1], -1
	s_cbranch_scc0 .Lpd_471
	s_add_i32 s0, s14, 0xfffffe01
	s_mul_hi_u32 s1, s0, 0x3e0f83e1
	s_lshr_b32 s23, s1, 8
	s_mul_i32 s15, s23, 0xfffffbe0
	s_add_i32 s15, s15, s0
	s_cmpk_gt_i32 s15, 0x15f
	s_mul_hi_u32 s27, s23, 0x2c00000
	s_mul_i32 s28, s23, 0x2c00000
	s_mov_b64 s[0:1], -1
	s_cbranch_scc0 .Lpd_468
	s_mov_b64 s[62:63], -1
	s_cmpk_gt_u32 s15, 0x2bf
	s_cbranch_scc0 .Lpd_466
	s_add_i32 s22, s15, 0xfffffd40
	v_readlane_b32 s0, v254, 49
	v_readlane_b32 s1, v254, 50
	s_add_u32 s44, s0, s28
	s_addc_u32 s45, s1, s27
	s_mul_i32 s1, s23, 0xb00000
	v_readlane_b32 s2, v254, 58
	s_mul_hi_u32 s0, s23, 0xb00000
	s_add_u32 s58, s2, s1
	v_readlane_b32 s1, v254, 59
	s_addc_u32 s59, s1, s0
	s_mov_b64 s[0:1], 0

; __device__ __forceinline__ unsigned pk4_fp8(float a, float b, float c, float d) { int w = 0; w = __builtin_amdgcn_cvt_pk_fp8_f32(a, b, w, false); w = __builtin_amdgcn_cvt_pk_fp8_f32(c, d, w, true); return (unsigned)w; }
; #define LAS __attribute__((address_space(3)))
; #define lane (lane_id())
; __device__ __forceinline__ void cv8_to_lds(const f32x4 (&v)[16], LAS unsigned char* T, int wave, int lane) {
;     unsigned d[16];
; #pragma unroll
;     for (int i = 0; i < 16; ++i) d[i] = pg8::pk4_fp8(v[i].x * 256.f, v[i].y * 256.f, v[i].z * 256.f, v[i].w * 256.f);
;     unsigned o[4][4];
; #pragma unroll
;     for (int q = 0; q < 4; ++q) { const unsigned a = d[4 * q], b = d[4 * q + 1], c = d[4 * q + 2], e = d[4 * q + 3];
;         const unsigned t0 = __builtin_amdgcn_perm(b, a, 0x05010400u), t1 = __builtin_amdgcn_perm(b, a, 0x07030602u), t2 = __builtin_amdgcn_perm(e, c, 0x05010400u), t3 = __builtin_amdgcn_perm(e, c, 0x07030602u);
;         o[0][q] = __builtin_amdgcn_perm(t2, t0, 0x05040100u); o[1][q] = __builtin_amdgcn_perm(t2, t0, 0x07060302u); o[2][q] = __builtin_amdgcn_perm(t3, t1, 0x05040100u); o[3][q] = __builtin_amdgcn_perm(t3, t1, 0x07060302u); }
; #pragma unroll
;     for (int j = 0; j < 4; ++j) { v4u w; w.x = o[j][0]; w.y = o[j][1]; w.z = o[j][2]; w.w = o[j][3];
;         *(LAS v4u*)(T + (4 * lane + j) * 128 + 16 * (wave ^ (lane & 7))) = w; }
; }
.Lpipe_xd_done:
	s_cbranch_scc1 .Lpa2_477
	s_ashr_i32 s57, s56, 31
	s_lshl_b64 s[0:1], s[56:57], 2
	s_add_u32 s0, s40, s0
	s_addc_u32 s1, s41, s1
	s_lshl_b32 s14, s96, 2
	s_load_dwordx16 s[40:55], s[0:1], s14 offset:0x0
	s_waitcnt lgkmcnt(0)
	s_mov_b32 s0, s43
	s_waitcnt vmcnt(28)
	v_pk_mul_f32 v[170:171], v[170:171], s[0:1] op_sel_hi:[1,0]
	v_pk_mul_f32 v[168:169], v[168:169], s[0:1] op_sel_hi:[1,0]
	s_mov_b32 s0, s45
	s_waitcnt vmcnt(26)
	v_pk_mul_f32 v[178:179], v[178:179], s[0:1] op_sel_hi:[1,0]
	v_pk_mul_f32 v[176:177], v[176:177], s[0:1] op_sel_hi:[1,0]
	s_mov_b32 s0, s47
	s_waitcnt vmcnt(24)
	v_pk_mul_f32 v[186:187], v[186:187], s[0:1] op_sel_hi:[1,0]
	v_pk_mul_f32 v[184:185], v[184:185], s[0:1] op_sel_hi:[1,0]
	s_mov_b32 s0, s49
	s_waitcnt vmcnt(22)
	v_pk_mul_f32 v[214:215], v[214:215], s[0:1] op_sel_hi:[1,0]
	v_pk_mul_f32 v[212:213], v[212:213], s[0:1] op_sel_hi:[1,0]
	s_mov_b32 s0, s51
	s_waitcnt vmcnt(20)
	v_pk_mul_f32 v[222:223], v[222:223], s[0:1] op_sel_hi:[1,0]
	v_pk_mul_f32 v[220:221], v[220:221], s[0:1] op_sel_hi:[1,0]
	s_mov_b32 s0, s53
	s_waitcnt vmcnt(18)
	v_pk_mul_f32 v[230:231], v[230:231], s[0:1] op_sel_hi:[1,0]
	v_pk_mul_f32 v[228:229], v[228:229], s[0:1] op_sel_hi:[1,0]
	s_mov_b32 s0, s55
	v_pk_mul_f32 v[158:159], v[158:159], s[40:41] op_sel_hi:[1,0]
	v_pk_mul_f32 v[156:157], v[156:157], s[40:41] op_sel_hi:[1,0]
	v_pk_mul_f32 v[162:163], v[162:163], s[40:41] op_sel:[0,1]
	v_pk_mul_f32 v[160:161], v[160:161], s[40:41] op_sel:[0,1]
	v_pk_mul_f32 v[166:167], v[166:167], s[42:43] op_sel_hi:[1,0]
	v_pk_mul_f32 v[164:165], v[164:165], s[42:43] op_sel_hi:[1,0]
	v_pk_mul_f32 v[174:175], v[174:175], s[44:45] op_sel_hi:[1,0]
	v_pk_mul_f32 v[172:173], v[172:173], s[44:45] op_sel_hi:[1,0]
	v_pk_mul_f32 v[182:183], v[182:183], s[46:47] op_sel_hi:[1,0]
	v_pk_mul_f32 v[180:181], v[180:181], s[46:47] op_sel_hi:[1,0]
	v_pk_mul_f32 v[210:211], v[210:211], s[48:49] op_sel_hi:[1,0]
	v_pk_mul_f32 v[208:209], v[208:209], s[48:49] op_sel_hi:[1,0]
	v_pk_mul_f32 v[218:219], v[218:219], s[50:51] op_sel_hi:[1,0]
	v_pk_mul_f32 v[216:217], v[216:217], s[50:51] op_sel_hi:[1,0]
	v_pk_mul_f32 v[226:227], v[226:227], s[52:53] op_sel_hi:[1,0]
	v_pk_mul_f32 v[224:225], v[224:225], s[52:53] op_sel_hi:[1,0]
	s_waitcnt vmcnt(17)
	v_pk_mul_f32 v[234:235], v[234:235], s[54:55] op_sel_hi:[1,0]
	v_pk_mul_f32 v[232:233], v[232:233], s[54:55] op_sel_hi:[1,0]
	s_waitcnt vmcnt(16)
	v_pk_mul_f32 v[238:239], v[238:239], s[0:1] op_sel_hi:[1,0]
	v_pk_mul_f32 v[236:237], v[236:237], s[0:1] op_sel_hi:[1,0]
.Lpa2_477:
	v_bitop3_b32 v240, v132, s95, 7 bitop3:0x6c
	s_xor_b64 s[40:41], s[76:77], -1
	v_lshlrev_b32_e32 v0, 9, v132
	v_lshlrev_b32_e32 v240, 4, v240
	v_add3_u32 v240, 0, v0, v240
	s_mov_b64 s[0:1], -1
	s_and_b64 vcc, exec, s[40:41]
	s_cbranch_vccz .Lpa2_479
	s_waitcnt vmcnt(31)
	v_mul_f32_e32 v0, 0x43800000, v156
	v_mul_f32_e32 v241, 0x43800000, v157
	v_mov_b32_e32 v136, v1
	v_cvt_pk_fp8_f32 v136, v0, v241
	s_waitcnt vmcnt(30)
	v_mul_f32_e32 v0, 0x43800000, v160
	v_mul_f32_e32 v241, 0x43800000, v161
	v_mov_b32_e32 v137, v1
	v_cvt_pk_fp8_f32 v137, v0, v241
	v_mul_f32_e32 v0, 0x43800000, v162
	v_mul_f32_e32 v241, 0x43800000, v163
	v_mov_b32_e32 v138, v1
	v_cvt_pk_fp8_f32 v137, v0, v241 op_sel:[0,0,1]
	s_waitcnt vmcnt(29)
	v_mul_f32_e32 v0, 0x43800000, v164
	v_mul_f32_e32 v241, 0x43800000, v165
	v_cvt_pk_fp8_f32 v138, v0, v241
	s_waitcnt vmcnt(28)
	v_mul_f32_e32 v0, 0x43800000, v168
	v_mul_f32_e32 v241, 0x43800000, v169
	v_mov_b32_e32 v139, v1
	v_cvt_pk_fp8_f32 v139, v0, v241
	v_mul_f32_e32 v0, 0x43800000, v170
	v_mul_f32_e32 v241, 0x43800000, v171
	v_mov_b32_e32 v140, v1
	v_cvt_pk_fp8_f32 v139, v0, v241 op_sel:[0,0,1]
	s_waitcnt vmcnt(27)
	v_mul_f32_e32 v0, 0x43800000, v172
	v_mul_f32_e32 v241, 0x43800000, v173
	v_cvt_pk_fp8_f32 v140, v0, v241
	s_waitcnt vmcnt(26)
	v_mul_f32_e32 v0, 0x43800000, v176
	v_mul_f32_e32 v241, 0x43800000, v177
	v_mov_b32_e32 v141, v1
	v_cvt_pk_fp8_f32 v141, v0, v241
	v_mul_f32_e32 v0, 0x43800000, v178
	v_mul_f32_e32 v241, 0x43800000, v179
	v_mov_b32_e32 v143, v1
	v_cvt_pk_fp8_f32 v141, v0, v241 op_sel:[0,0,1]
	s_waitcnt vmcnt(25)
	v_mul_f32_e32 v0, 0x43800000, v180
	v_mul_f32_e32 v241, 0x43800000, v181
	v_cvt_pk_fp8_f32 v143, v0, v241
	s_waitcnt vmcnt(24)
	v_mul_f32_e32 v0, 0x43800000, v184
	v_mul_f32_e32 v241, 0x43800000, v185
	v_mov_b32_e32 v144, v1
	v_cvt_pk_fp8_f32 v144, v0, v241
	v_mul_f32_e32 v0, 0x43800000, v186
	v_mul_f32_e32 v241, 0x43800000, v187
	v_mov_b32_e32 v145, v1
	v_cvt_pk_fp8_f32 v144, v0, v241 op_sel:[0,0,1]
	s_waitcnt vmcnt(23)
	v_mul_f32_e32 v0, 0x43800000, v208
	v_mul_f32_e32 v241, 0x43800000, v209
	v_cvt_pk_fp8_f32 v145, v0, v241
	s_waitcnt vmcnt(22)
	v_mul_f32_e32 v0, 0x43800000, v212
	v_mul_f32_e32 v241, 0x43800000, v213
	v_mov_b32_e32 v148, v1
	v_cvt_pk_fp8_f32 v148, v0, v241
	v_mul_f32_e32 v0, 0x43800000, v214
	v_mul_f32_e32 v241, 0x43800000, v215
	v_mov_b32_e32 v149, v1
	v_cvt_pk_fp8_f32 v148, v0, v241 op_sel:[0,0,1]
	s_waitcnt vmcnt(21)
	v_mul_f32_e32 v0, 0x43800000, v216
	v_mul_f32_e32 v241, 0x43800000, v217
	v_cvt_pk_fp8_f32 v149, v0, v241
	s_waitcnt vmcnt(20)
	v_mul_f32_e32 v0, 0x43800000, v220
	v_mul_f32_e32 v241, 0x43800000, v221
	v_mov_b32_e32 v150, v1
	v_cvt_pk_fp8_f32 v150, v0, v241
	v_mul_f32_e32 v0, 0x43800000, v222
	v_mul_f32_e32 v241, 0x43800000, v223
	v_mov_b32_e32 v151, v1
	v_cvt_pk_fp8_f32 v150, v0, v241 op_sel:[0,0,1]
	s_waitcnt vmcnt(19)
	v_mul_f32_e32 v0, 0x43800000, v224
	v_mul_f32_e32 v241, 0x43800000, v225
	v_cvt_pk_fp8_f32 v151, v0, v241
	s_waitcnt vmcnt(18)
; __device__ __forceinline__ unsigned pk4_fp8(float a, float b, float c, float d) { int w = 0; w = __builtin_amdgcn_cvt_pk_fp8_f32(a, b, w, false); w = __builtin_amdgcn_cvt_pk_fp8_f32(c, d, w, true); return (unsigned)w; }
; #define LAS __attribute__((address_space(3)))
; #define lane (lane_id())
; __device__ __forceinline__ void cv8_to_lds(const f32x4 (&v)[16], LAS unsigned char* T, int wave, int lane) {
;     unsigned d[16];
; #pragma unroll
;     for (int i = 0; i < 16; ++i) d[i] = pg8::pk4_fp8(v[i].x * 256.f, v[i].y * 256.f, v[i].z * 256.f, v[i].w * 256.f);
;     unsigned o[4][4];
; #pragma unroll
;     for (int q = 0; q < 4; ++q) { const unsigned a = d[4 * q], b = d[4 * q + 1], c = d[4 * q + 2], e = d[4 * q + 3];
;         const unsigned t0 = __builtin_amdgcn_perm(b, a, 0x05010400u), t1 = __builtin_amdgcn_perm(b, a, 0x07030602u), t2 = __builtin_amdgcn_perm(e, c, 0x05010400u), t3 = __builtin_amdgcn_perm(e, c, 0x07030602u);
;         o[0][q] = __builtin_amdgcn_perm(t2, t0, 0x05040100u); o[1][q] = __builtin_amdgcn_perm(t2, t0, 0x07060302u); o[2][q] = __builtin_amdgcn_perm(t3, t1, 0x05040100u); o[3][q] = __builtin_amdgcn_perm(t3, t1, 0x07060302u); }
; #pragma unroll
;     for (int j = 0; j < 4; ++j) { v4u w; w.x = o[j][0]; w.y = o[j][1]; w.z = o[j][2]; w.w = o[j][3];
;         *(LAS v4u*)(T + (4 * lane + j) * 128 + 16 * (wave ^ (lane & 7))) = w; }
; }
	v_mul_f32_e32 v0, 0x43800000, v228
	v_mul_f32_e32 v241, 0x43800000, v229
	v_mov_b32_e32 v152, v1
	v_cvt_pk_fp8_f32 v152, v0, v241
	v_mul_f32_e32 v134, 0x43800000, v158
	v_mul_f32_e32 v135, 0x43800000, v159
	v_cvt_pk_fp8_f32 v136, v134, v135 op_sel:[0,0,1]
	v_mul_f32_e32 v134, 0x43800000, v166
	v_mul_f32_e32 v135, 0x43800000, v167
	v_mul_f32_e32 v0, 0x43800000, v230
	v_mul_f32_e32 v241, 0x43800000, v231
	v_cvt_pk_fp8_f32 v138, v134, v135 op_sel:[0,0,1]
	v_mul_f32_e32 v134, 0x43800000, v174
	v_mul_f32_e32 v135, 0x43800000, v175
	v_cvt_pk_fp8_f32 v152, v0, v241 op_sel:[0,0,1]
	s_waitcnt vmcnt(17)
	v_mul_f32_e32 v0, 0x43800000, v232
	v_mul_f32_e32 v241, 0x43800000, v233
	v_mov_b32_e32 v153, v1
	v_cvt_pk_fp8_f32 v140, v134, v135 op_sel:[0,0,1]
	v_mul_f32_e32 v134, 0x43800000, v182
	v_mul_f32_e32 v135, 0x43800000, v183
	v_cvt_pk_fp8_f32 v153, v0, v241
	s_waitcnt vmcnt(16)
	v_mul_f32_e32 v0, 0x43800000, v236
	v_mul_f32_e32 v241, 0x43800000, v237
	v_mov_b32_e32 v154, v1
	v_cvt_pk_fp8_f32 v143, v134, v135 op_sel:[0,0,1]
	v_mul_f32_e32 v134, 0x43800000, v210
	v_mul_f32_e32 v135, 0x43800000, v211
	v_cvt_pk_fp8_f32 v154, v0, v241
	v_cvt_pk_fp8_f32 v145, v134, v135 op_sel:[0,0,1]
	v_mul_f32_e32 v134, 0x43800000, v218
	v_mul_f32_e32 v135, 0x43800000, v219
	v_cvt_pk_fp8_f32 v149, v134, v135 op_sel:[0,0,1]
	v_mul_f32_e32 v134, 0x43800000, v226
	v_mul_f32_e32 v135, 0x43800000, v227
	v_cvt_pk_fp8_f32 v151, v134, v135 op_sel:[0,0,1]
	v_mul_f32_e32 v134, 0x43800000, v234
	v_mul_f32_e32 v135, 0x43800000, v235
	v_mul_f32_e32 v0, 0x43800000, v238
	v_mul_f32_e32 v241, 0x43800000, v239
	v_cvt_pk_fp8_f32 v153, v134, v135 op_sel:[0,0,1]
	v_cvt_pk_fp8_f32 v154, v0, v241 op_sel:[0,0,1]
	s_mov_b32 s0, 0x5010400
	s_mov_b32 s1, 0x7030602
	v_perm_b32 v0, v137, v136, s0
	v_perm_b32 v241, v137, v136, s1
	v_perm_b32 v135, v139, v138, s0
	v_perm_b32 v136, v139, v138, s1
	s_mov_b32 s3, 0x5040100
	s_mov_b32 s2, 0x7060302
	v_perm_b32 v134, v135, v0, s3
	v_perm_b32 v138, v135, v0, s2
	v_perm_b32 v142, v136, v241, s3
	v_perm_b32 v146, v136, v241, s2
	v_perm_b32 v0, v141, v140, s0
	v_perm_b32 v241, v141, v140, s1
	v_perm_b32 v136, v144, v143, s0
	v_perm_b32 v137, v144, v143, s1
	v_perm_b32 v135, v136, v0, s3
	v_perm_b32 v139, v136, v0, s2
	v_perm_b32 v143, v137, v241, s3
	v_perm_b32 v147, v137, v241, s2
	v_perm_b32 v0, v148, v145, s0
	v_perm_b32 v241, v148, v145, s1
	v_perm_b32 v137, v150, v149, s0
	v_perm_b32 v141, v150, v149, s1
	v_perm_b32 v136, v137, v0, s3
	v_perm_b32 v140, v137, v0, s2
	v_perm_b32 v144, v141, v241, s3
	v_perm_b32 v148, v141, v241, s2
	v_perm_b32 v0, v152, v151, s0
	v_perm_b32 v141, v154, v153, s0
	v_perm_b32 v241, v152, v151, s1
	v_perm_b32 v149, v154, v153, s1
	v_perm_b32 v137, v141, v0, s3
	v_perm_b32 v141, v141, v0, s2
	v_perm_b32 v145, v149, v241, s3
	v_perm_b32 v149, v149, v241, s2
	ds_write_b128 v240, v[134:137]
	ds_write_b128 v240, v[138:141] offset:128
	ds_write_b128 v240, v[142:145] offset:256
	ds_write_b128 v240, v[146:149] offset:384
	s_waitcnt lgkmcnt(0)
	s_waitcnt lgkmcnt(0)
	s_barrier
	s_mov_b64 s[0:1], 0
.Lpa2_479:
	v_xor_b32_e32 v0, s95, v132
	v_lshlrev_b32_e32 v0, 4, v0
	v_readlane_b32 s76, v254, 30
	s_andn2_b64 vcc, exec, s[0:1]
	v_add_u32_e32 v241, s97, v0
	v_readlane_b32 s77, v254, 31
	v_readlane_b32 s78, v254, 32
	v_readlane_b32 s79, v254, 33
	s_cbranch_vccnz .Lpa2_481
	s_waitcnt vmcnt(31)
	ds_write_b128 v241, v[156:159]
	s_waitcnt vmcnt(30)
	ds_write_b128 v241, v[160:163] offset:1040
	s_waitcnt vmcnt(29)
	ds_write_b128 v241, v[164:167] offset:2080
	s_waitcnt vmcnt(28)
	ds_write_b128 v241, v[168:171] offset:3120
	s_waitcnt vmcnt(27)
	ds_write_b128 v241, v[172:175] offset:4160
	s_waitcnt vmcnt(26)
	ds_write_b128 v241, v[176:179] offset:5200
	s_waitcnt vmcnt(25)
	ds_write_b128 v241, v[180:183] offset:6240
	s_waitcnt vmcnt(24)
	ds_write_b128 v241, v[184:187] offset:7280
	s_waitcnt vmcnt(23)
	ds_write_b128 v241, v[208:211] offset:8320
	s_waitcnt vmcnt(22)
	ds_write_b128 v241, v[212:215] offset:9360
	s_waitcnt vmcnt(21)
	ds_write_b128 v241, v[216:219] offset:10400
	s_waitcnt vmcnt(20)
	ds_write_b128 v241, v[220:223] offset:11440
	s_waitcnt vmcnt(19)
	ds_write_b128 v241, v[224:227] offset:12480
	s_waitcnt vmcnt(18)
	ds_write_b128 v241, v[228:231] offset:13520
	s_waitcnt vmcnt(17)
	ds_write_b128 v241, v[232:235] offset:14560
	s_waitcnt vmcnt(16)
	ds_write_b128 v241, v[236:239] offset:15600
	s_waitcnt lgkmcnt(0)
	s_waitcnt lgkmcnt(0)
	s_barrier
; #define GAS __attribute__((address_space(1)))
; #define LAS __attribute__((address_space(3)))
; __device__ __forceinline__ void cv8_out(const CvTile& cur, const LAS unsigned char* T, int tid_) {
;     const int nbl = cur.N / 256, kb = cur.r / nbl, nb = cur.r - kb * nbl;
; #pragma unroll
;     for (int i = 0; i < 4; ++i) { const int p = tid_ + 512 * i, c = p & 7, n = p >> 3, nn = 256 * nb + n;
;         const int drow = (cur.mode == 0) ? nn : (256 * (nn >> 7) + (nn & 127) + (cur.mode == 2 ? 128 : 0));
;         const v4u w = *(const LAS v4u*)(T + n * 128 + 16 * (c ^ ((n >> 2) & 7)));
;         __builtin_nontemporal_store(w, (GAS v4u*)(cur.WT + (size_t)drow * cur.K + 128 * kb + 16 * c)); }
; }
.Lpa2_481:
	s_waitcnt vmcnt(31)
	v_add_u32_e32 v156, s94, v132
	v_lshrrev_b32_e32 v0, 5, v156
	v_xor_b32_e32 v0, v0, v132
	v_lshlrev_b32_e32 v0, 4, v0
	v_and_b32_e32 v0, 0x70, v0
	v_add_u32_e32 v157, 0x200, v156
	v_add_u32_e32 v158, 0x400, v156
	v_add_u32_e32 v159, 0x600, v156
	s_waitcnt vmcnt(23)
	v_add_u32_e32 v211, 0, v0
	v_lshlrev_b32_e32 v0, 4, v132
	s_waitcnt vmcnt(22)
	v_ashrrev_i32_e32 v212, 3, v156
	v_ashrrev_i32_e32 v208, 3, v157
	v_ashrrev_i32_e32 v184, 3, v158
	v_ashrrev_i32_e32 v181, 3, v159
	v_and_b32_e32 v0, 0x70, v0
	v_and_b32_e32 v210, 0x7f, v212
	v_lshlrev_b32_e32 v209, 7, v212
	v_and_b32_e32 v187, 0x7f, v208
	v_lshlrev_b32_e32 v186, 7, v208
	v_and_b32_e32 v183, 0x7f, v184
	v_lshlrev_b32_e32 v182, 7, v184
	v_and_b32_e32 v180, 0x7f, v181
	v_lshlrev_b32_e32 v179, 7, v181
	s_andn2_b64 vcc, exec, s[40:41]
	s_ashr_i32 s57, s56, 31
	s_cbranch_vccnz .Lpa2_484
	v_add_u32_e32 v160, s84, v212
	v_lshlrev_b32_e32 v161, 1, v160
	v_and_b32_e32 v161, 0xffffff00, v161
	v_or3_b32 v161, v210, v161, s19
	v_cndmask_b32_e64 v166, v161, v160, s[72:73]
	v_add_u32_e32 v160, v211, v209
	v_ashrrev_i32_e32 v164, 31, v166
	ds_read_b128 v[160:163], v160
	v_mul_lo_u32 v168, s68, v164
	v_mov_b64_e32 v[164:165], s[66:67]
	v_mul_lo_u32 v169, s69, v166
	v_mad_u64_u32 v[166:167], s[0:1], s68, v166, v[164:165]
	v_add3_u32 v167, v169, v167, v168
	v_lshl_add_u64 v[166:167], v[166:167], 0, s[56:57]
	v_lshl_add_u64 v[166:167], v[166:167], 0, v[0:1]
	s_waitcnt lgkmcnt(0)
	global_store_dwordx4 v[166:167], v[160:163], off nt
	s_mov_b64 s[14:15], 0
	s_and_b64 vcc, exec, s[74:75]
	v_add_u32_e32 v160, s84, v208
	v_lshlrev_b32_e32 v161, 1, v160
	v_and_b32_e32 v161, 0xffffff00, v161
	v_or3_b32 v161, v187, v161, s19
	v_cndmask_b32_e64 v166, v161, v160, s[72:73]
	v_add_u32_e32 v160, v211, v186
	ds_read_b128 v[160:163], v160
	v_ashrrev_i32_e32 v167, 31, v166
	v_mul_lo_u32 v168, s68, v167
	v_mul_lo_u32 v169, s69, v166
	v_mad_u64_u32 v[166:167], s[0:1], s68, v166, v[164:165]
	v_add3_u32 v167, v169, v167, v168
	v_lshl_add_u64 v[166:167], v[166:167], 0, s[56:57]
	v_lshl_add_u64 v[166:167], v[166:167], 0, v[0:1]
	s_waitcnt lgkmcnt(0)
	global_store_dwordx4 v[166:167], v[160:163], off nt
	s_nop 1
	v_add_u32_e32 v160, s84, v184
	v_lshlrev_b32_e32 v161, 1, v160
	v_and_b32_e32 v161, 0xffffff00, v161
	v_or3_b32 v161, v183, v161, s19
	v_cndmask_b32_e64 v166, v161, v160, s[72:73]
	v_add_u32_e32 v160, v211, v182
	ds_read_b128 v[160:163], v160
	v_ashrrev_i32_e32 v167, 31, v166
	v_mul_lo_u32 v168, s68, v167
	v_mul_lo_u32 v169, s69, v166
	v_mad_u64_u32 v[166:167], s[0:1], s68, v166, v[164:165]
	v_add3_u32 v167, v169, v167, v168
	v_lshl_add_u64 v[166:167], v[166:167], 0, s[56:57]
	v_lshl_add_u64 v[166:167], v[166:167], 0, v[0:1]
	s_waitcnt lgkmcnt(0)
	global_store_dwordx4 v[166:167], v[160:163], off nt
	s_nop 1
	v_add_u32_e32 v160, s84, v181
	v_lshlrev_b32_e32 v161, 1, v160
	v_and_b32_e32 v161, 0xffffff00, v161
	v_or3_b32 v161, v180, v161, s19
	v_cndmask_b32_e64 v166, v161, v160, s[72:73]
	v_add_u32_e32 v160, v211, v179
	ds_read_b128 v[160:163], v160
	v_ashrrev_i32_e32 v167, 31, v166
	v_mul_lo_u32 v167, s68, v167
	v_mul_lo_u32 v168, s69, v166
	v_mad_u64_u32 v[164:165], s[0:1], s68, v166, v[164:165]
	v_add3_u32 v165, v168, v165, v167
	v_lshl_add_u64 v[164:165], v[164:165], 0, s[56:57]
	v_lshl_add_u64 v[164:165], v[164:165], 0, v[0:1]
	s_mov_b64 s[0:1], 0
	s_waitcnt lgkmcnt(0)
	global_store_dwordx4 v[164:165], v[160:163], off nt
	s_cbranch_vccz .Lpa2_485
	s_waitcnt lgkmcnt(0)
	s_mov_b64 s[0:1], -1
	s_barrier
	s_branch .Lpa2_485

; #define GAS __attribute__((address_space(1)))
; #define LAS __attribute__((address_space(3)))
; __device__ __forceinline__ unsigned pk2(float lo, float hi) { return f2bf(lo) | (f2bf(hi) << 16); }
; __device__ __forceinline__ void cv_tile_out(const CvTile& cur, LAS float* S, int tid_) {
;     ...
; #pragma unroll
;         for (int i = 0; i < 8; ++i) { const int p = tid_ + 512 * i, kc = p & 15, n = p >> 4, nn = 256 * nb + n;
;             const int drow = (cur.mode == 0) ? nn : (256 * (nn >> 7) + (nn & 127) + (cur.mode == 2 ? 128 : 0));
;             const LAS float* sp = S + (8 * kc) * LS + (n ^ (4 * (kc >> 1))); v4u o;
;             o.x = pk2(sp[0], sp[LS]); o.y = pk2(sp[2 * LS], sp[3 * LS]); o.z = pk2(sp[4 * LS], sp[5 * LS]); o.w = pk2(sp[6 * LS], sp[7 * LS]);
;             *(GAS v4u*)((bf16*)cur.WT + (size_t)drow * cur.K + 128 * kb + 8 * kc) = o; } }
.Lpa2_485:
	s_nop 0
	v_and_b32_e32 v160, 15, v132
	s_movk_i32 s22, 0x2080
	s_waitcnt vmcnt(21)
	v_lshlrev_b32_e32 v217, 1, v132
	v_ashrrev_i32_e32 v178, 4, v157
	v_mad_u32_u24 v216, v160, s22, 0
	v_bitop3_b32 v157, v178, v217, 28 bitop3:0x78
	v_ashrrev_i32_e32 v175, 4, v158
	v_lshl_add_u32 v176, v157, 2, v216
	v_bitop3_b32 v157, v175, v217, 28 bitop3:0x78
	v_ashrrev_i32_e32 v172, 4, v159
	v_lshl_add_u32 v173, v157, 2, v216
	v_bitop3_b32 v157, v172, v217, 28 bitop3:0x78
	v_lshl_add_u32 v170, v157, 2, v216
	v_add_u32_e32 v157, 0x800, v156
	v_ashrrev_i32_e32 v169, 4, v157
	v_bitop3_b32 v157, v169, v217, 28 bitop3:0x78
	v_lshl_add_u32 v167, v157, 2, v216
	v_add_u32_e32 v157, 0xa00, v156
	v_ashrrev_i32_e32 v166, 4, v157
	v_ashrrev_i32_e32 v214, 4, v156
	v_bitop3_b32 v157, v166, v217, 28 bitop3:0x78
	v_lshlrev_b32_e32 v215, 3, v160
	v_bitop3_b32 v160, v217, v214, 28 bitop3:0x6c
	v_lshl_add_u32 v164, v157, 2, v216
	v_add_u32_e32 v157, 0xc00, v156
	v_add_u32_e32 v156, 0xe00, v156
	v_lshl_add_u32 v185, v160, 2, v216
	v_ashrrev_i32_e32 v163, 4, v157
	v_ashrrev_i32_e32 v160, 4, v156
	v_bitop3_b32 v157, v163, v217, 28 bitop3:0x78
	v_bitop3_b32 v156, v160, v217, 28 bitop3:0x78
	v_and_b32_e32 v213, 0x7f, v214
	v_and_b32_e32 v177, 0x7f, v178
	v_and_b32_e32 v174, 0x7f, v175
	v_and_b32_e32 v171, 0x7f, v172
	v_and_b32_e32 v168, 0x7f, v169
	v_and_b32_e32 v165, 0x7f, v166
	v_and_b32_e32 v162, 0x7f, v163
	v_lshl_add_u32 v161, v157, 2, v216
	v_and_b32_e32 v159, 0x7f, v160
	v_lshl_add_u32 v158, v156, 2, v216
	s_mov_b32 s22, 0x8000
	s_and_b64 vcc, exec, s[14:15]
	v_lshlrev_b32_e32 v156, 1, v215
	s_cbranch_vccz .Lpa2_487
	v_add_u32_e32 v157, s84, v214
	v_lshlrev_b32_e32 v215, 1, v157
	v_and_b32_e32 v215, 0xffffff00, v215
	v_or3_b32 v215, v213, v215, s19
	v_cndmask_b32_e64 v157, v215, v157, s[72:73]
	ds_read_b32 v215, v185
	ds_read_b32 v216, v185 offset:1040
	s_waitcnt vmcnt(20)
	v_mul_lo_u32 v222, s69, v157
	s_lshl_b64 s[40:41], s[56:57], 1
	s_mov_b32 s22, 0
	s_waitcnt lgkmcnt(1)
	v_bfe_u32 v217, v215, 16, 1
	v_add3_u32 v215, v215, v217, s10
	s_waitcnt lgkmcnt(0)
	v_bfe_u32 v217, v216, 16, 1
	v_lshrrev_b32_e32 v215, 16, v215
	v_add3_u32 v216, v216, v217, s10
	v_and_or_b32 v216, v216, s11, v215
	ds_read_b32 v215, v185 offset:2080
	ds_read_b32 v217, v185 offset:3120
	s_waitcnt lgkmcnt(1)
	v_bfe_u32 v218, v215, 16, 1
	v_add3_u32 v215, v215, v218, s10
	s_waitcnt lgkmcnt(0)
	v_bfe_u32 v218, v217, 16, 1
	v_lshrrev_b32_e32 v215, 16, v215
	v_add3_u32 v217, v217, v218, s10
	v_and_or_b32 v217, v217, s11, v215
	ds_read_b32 v215, v185 offset:4160
	ds_read_b32 v218, v185 offset:5200
	s_waitcnt lgkmcnt(1)
	v_bfe_u32 v219, v215, 16, 1
	v_add3_u32 v215, v215, v219, s10
	s_waitcnt lgkmcnt(0)
	v_bfe_u32 v219, v218, 16, 1
	v_lshrrev_b32_e32 v215, 16, v215
	v_add3_u32 v218, v218, v219, s10
	v_and_or_b32 v218, v218, s11, v215
	ds_read_b32 v215, v185 offset:6240
	ds_read_b32 v219, v185 offset:7280
	s_waitcnt lgkmcnt(1)
	v_bfe_u32 v220, v215, 16, 1
	v_add3_u32 v215, v215, v220, s10
	s_waitcnt lgkmcnt(0)
	v_bfe_u32 v220, v219, 16, 1
	v_lshrrev_b32_e32 v215, 16, v215
	v_add3_u32 v219, v219, v220, s10
	v_and_or_b32 v219, v219, s11, v215
	v_ashrrev_i32_e32 v215, 31, v157
	v_mul_lo_u32 v215, s68, v215
	v_mad_u64_u32 v[220:221], s[0:1], s68, v157, 0
	v_add3_u32 v221, v221, v215, v222
	v_lshl_add_u64 v[220:221], v[220:221], 1, s[66:67]
	v_lshl_add_u64 v[220:221], v[220:221], 0, s[40:41]
	v_mov_b32_e32 v157, v1
	v_lshl_add_u64 v[220:221], v[220:221], 0, v[156:157]
	v_add_u32_e32 v215, s84, v178
	global_store_dwordx4 v[220:221], v[216:219], off
	s_nop 1
	v_lshlrev_b32_e32 v216, 1, v215
	v_and_b32_e32 v216, 0xffffff00, v216
	v_or3_b32 v216, v177, v216, s19
	v_cndmask_b32_e64 v215, v216, v215, s[72:73]
	ds_read_b32 v216, v176
	ds_read_b32 v217, v176 offset:1040
	v_mul_lo_u32 v223, s69, v215
	s_waitcnt lgkmcnt(1)
	v_bfe_u32 v218, v216, 16, 1
	v_add3_u32 v216, v216, v218, s10
	s_waitcnt lgkmcnt(0)
	v_bfe_u32 v218, v217, 16, 1
	v_lshrrev_b32_e32 v216, 16, v216
	v_add3_u32 v217, v217, v218, s10
	v_and_or_b32 v216, v217, s11, v216
	ds_read_b32 v217, v176 offset:2080
	ds_read_b32 v218, v176 offset:3120
	s_waitcnt lgkmcnt(1)
	v_bfe_u32 v219, v217, 16, 1
	v_add3_u32 v217, v217, v219, s10
	s_waitcnt lgkmcnt(0)
	v_bfe_u32 v219, v218, 16, 1
	v_lshrrev_b32_e32 v217, 16, v217
	v_add3_u32 v218, v218, v219, s10
	v_and_or_b32 v217, v218, s11, v217
	ds_read_b32 v218, v176 offset:4160
	ds_read_b32 v219, v176 offset:5200
	s_waitcnt lgkmcnt(1)
	v_bfe_u32 v220, v218, 16, 1
	v_add3_u32 v218, v218, v220, s10
	s_waitcnt lgkmcnt(0)
	v_bfe_u32 v220, v219, 16, 1
	v_lshrrev_b32_e32 v218, 16, v218
	v_add3_u32 v219, v219, v220, s10
	v_and_or_b32 v218, v219, s11, v218
	ds_read_b32 v219, v176 offset:6240
	ds_read_b32 v220, v176 offset:7280
	s_waitcnt lgkmcnt(1)
	v_bfe_u32 v221, v219, 16, 1
	v_add3_u32 v219, v219, v221, s10
	s_waitcnt lgkmcnt(0)
	v_bfe_u32 v221, v220, 16, 1
	v_lshrrev_b32_e32 v219, 16, v219
	v_add3_u32 v220, v220, v221, s10
	v_and_or_b32 v219, v220, s11, v219
	v_ashrrev_i32_e32 v220, 31, v215
	v_mul_lo_u32 v222, s68, v220
	v_mad_u64_u32 v[220:221], s[0:1], s68, v215, 0
	v_add3_u32 v221, v221, v222, v223
	v_lshl_add_u64 v[220:221], v[220:221], 1, s[66:67]
	v_lshl_add_u64 v[220:221], v[220:221], 0, s[40:41]
	v_lshl_add_u64 v[220:221], v[220:221], 0, v[156:157]
	v_add_u32_e32 v215, s84, v175
	global_store_dwordx4 v[220:221], v[216:219], off
	s_nop 1
	v_lshlrev_b32_e32 v216, 1, v215
	v_and_b32_e32 v216, 0xffffff00, v216
	v_or3_b32 v216, v174, v216, s19
	v_cndmask_b32_e64 v215, v216, v215, s[72:73]
	ds_read_b32 v216, v173
	ds_read_b32 v217, v173 offset:1040
	v_mul_lo_u32 v223, s69, v215
	s_waitcnt lgkmcnt(1)
; #define GAS __attribute__((address_space(1)))
; #define LAS __attribute__((address_space(3)))
; __device__ __forceinline__ unsigned pk2(float lo, float hi) { return f2bf(lo) | (f2bf(hi) << 16); }
; __device__ __forceinline__ void cv_tile_out(const CvTile& cur, LAS float* S, int tid_) {
;     ...
; #pragma unroll
;         for (int i = 0; i < 8; ++i) { const int p = tid_ + 512 * i, kc = p & 15, n = p >> 4, nn = 256 * nb + n;
;             const int drow = (cur.mode == 0) ? nn : (256 * (nn >> 7) + (nn & 127) + (cur.mode == 2 ? 128 : 0));
;             const LAS float* sp = S + (8 * kc) * LS + (n ^ (4 * (kc >> 1))); v4u o;
;             o.x = pk2(sp[0], sp[LS]); o.y = pk2(sp[2 * LS], sp[3 * LS]); o.z = pk2(sp[4 * LS], sp[5 * LS]); o.w = pk2(sp[6 * LS], sp[7 * LS]);
;             *(GAS v4u*)((bf16*)cur.WT + (size_t)drow * cur.K + 128 * kb + 8 * kc) = o; } }
	v_bfe_u32 v218, v216, 16, 1
	v_add3_u32 v216, v216, v218, s10
	s_waitcnt lgkmcnt(0)
	v_bfe_u32 v218, v217, 16, 1
	v_lshrrev_b32_e32 v216, 16, v216
	v_add3_u32 v217, v217, v218, s10
	v_and_or_b32 v216, v217, s11, v216
	ds_read_b32 v217, v173 offset:2080
	ds_read_b32 v218, v173 offset:3120
	s_waitcnt lgkmcnt(1)
	v_bfe_u32 v219, v217, 16, 1
	v_add3_u32 v217, v217, v219, s10
	s_waitcnt lgkmcnt(0)
	v_bfe_u32 v219, v218, 16, 1
	v_lshrrev_b32_e32 v217, 16, v217
	v_add3_u32 v218, v218, v219, s10
	v_and_or_b32 v217, v218, s11, v217
	ds_read_b32 v218, v173 offset:4160
	ds_read_b32 v219, v173 offset:5200
	s_waitcnt lgkmcnt(1)
	v_bfe_u32 v220, v218, 16, 1
	v_add3_u32 v218, v218, v220, s10
	s_waitcnt lgkmcnt(0)
	v_bfe_u32 v220, v219, 16, 1
	v_lshrrev_b32_e32 v218, 16, v218
	v_add3_u32 v219, v219, v220, s10
	v_and_or_b32 v218, v219, s11, v218
	ds_read_b32 v219, v173 offset:6240
	ds_read_b32 v220, v173 offset:7280
	s_waitcnt lgkmcnt(1)
	v_bfe_u32 v221, v219, 16, 1
	v_add3_u32 v219, v219, v221, s10
	s_waitcnt lgkmcnt(0)
	v_bfe_u32 v221, v220, 16, 1
	v_lshrrev_b32_e32 v219, 16, v219
	v_add3_u32 v220, v220, v221, s10
	v_and_or_b32 v219, v220, s11, v219
	v_ashrrev_i32_e32 v220, 31, v215
	v_mul_lo_u32 v222, s68, v220
	v_mad_u64_u32 v[220:221], s[0:1], s68, v215, 0
	v_add3_u32 v221, v221, v222, v223
	v_lshl_add_u64 v[220:221], v[220:221], 1, s[66:67]
	v_lshl_add_u64 v[220:221], v[220:221], 0, s[40:41]
	v_lshl_add_u64 v[220:221], v[220:221], 0, v[156:157]
	v_add_u32_e32 v215, s84, v172
	global_store_dwordx4 v[220:221], v[216:219], off
	s_nop 1
	v_lshlrev_b32_e32 v216, 1, v215
	v_and_b32_e32 v216, 0xffffff00, v216
	v_or3_b32 v216, v171, v216, s19
	v_cndmask_b32_e64 v215, v216, v215, s[72:73]
	ds_read_b32 v216, v170
	ds_read_b32 v217, v170 offset:1040
	v_mul_lo_u32 v223, s69, v215
	s_waitcnt lgkmcnt(1)
	v_bfe_u32 v218, v216, 16, 1
	v_add3_u32 v216, v216, v218, s10
	s_waitcnt lgkmcnt(0)
	v_bfe_u32 v218, v217, 16, 1
	v_lshrrev_b32_e32 v216, 16, v216
	v_add3_u32 v217, v217, v218, s10
	v_and_or_b32 v216, v217, s11, v216
	ds_read_b32 v217, v170 offset:2080
	ds_read_b32 v218, v170 offset:3120
	s_waitcnt lgkmcnt(1)
	v_bfe_u32 v219, v217, 16, 1
	v_add3_u32 v217, v217, v219, s10
	s_waitcnt lgkmcnt(0)
	v_bfe_u32 v219, v218, 16, 1
	v_lshrrev_b32_e32 v217, 16, v217
	v_add3_u32 v218, v218, v219, s10
	v_and_or_b32 v217, v218, s11, v217
	ds_read_b32 v218, v170 offset:4160
	ds_read_b32 v219, v170 offset:5200
	s_waitcnt lgkmcnt(1)
	v_bfe_u32 v220, v218, 16, 1
	v_add3_u32 v218, v218, v220, s10
	s_waitcnt lgkmcnt(0)
	v_bfe_u32 v220, v219, 16, 1
	v_lshrrev_b32_e32 v218, 16, v218
	v_add3_u32 v219, v219, v220, s10
	v_and_or_b32 v218, v219, s11, v218
	ds_read_b32 v219, v170 offset:6240
	ds_read_b32 v220, v170 offset:7280
	s_waitcnt lgkmcnt(1)
	v_bfe_u32 v221, v219, 16, 1
	v_add3_u32 v219, v219, v221, s10
	s_waitcnt lgkmcnt(0)
	v_bfe_u32 v221, v220, 16, 1
	v_lshrrev_b32_e32 v219, 16, v219
	v_add3_u32 v220, v220, v221, s10
	v_and_or_b32 v219, v220, s11, v219
	v_ashrrev_i32_e32 v220, 31, v215
	v_mul_lo_u32 v222, s68, v220
	v_mad_u64_u32 v[220:221], s[0:1], s68, v215, 0
	v_add3_u32 v221, v221, v222, v223
	v_lshl_add_u64 v[220:221], v[220:221], 1, s[66:67]
	v_lshl_add_u64 v[220:221], v[220:221], 0, s[40:41]
	v_lshl_add_u64 v[220:221], v[220:221], 0, v[156:157]
	v_add_u32_e32 v215, s84, v169
	global_store_dwordx4 v[220:221], v[216:219], off
	s_nop 1
	v_lshlrev_b32_e32 v216, 1, v215
	v_and_b32_e32 v216, 0xffffff00, v216
	v_or3_b32 v216, v168, v216, s19
	v_cndmask_b32_e64 v215, v216, v215, s[72:73]
	ds_read_b32 v216, v167
	ds_read_b32 v217, v167 offset:1040
	v_mul_lo_u32 v223, s69, v215
	s_waitcnt lgkmcnt(1)
	v_bfe_u32 v218, v216, 16, 1
	v_add3_u32 v216, v216, v218, s10
	s_waitcnt lgkmcnt(0)
	v_bfe_u32 v218, v217, 16, 1
	v_lshrrev_b32_e32 v216, 16, v216
	v_add3_u32 v217, v217, v218, s10
	v_and_or_b32 v216, v217, s11, v216
	ds_read_b32 v217, v167 offset:2080
	ds_read_b32 v218, v167 offset:3120
	s_waitcnt lgkmcnt(1)
	v_bfe_u32 v219, v217, 16, 1
	v_add3_u32 v217, v217, v219, s10
	s_waitcnt lgkmcnt(0)
	v_bfe_u32 v219, v218, 16, 1
	v_lshrrev_b32_e32 v217, 16, v217
	v_add3_u32 v218, v218, v219, s10
	v_and_or_b32 v217, v218, s11, v217
	ds_read_b32 v218, v167 offset:4160
	ds_read_b32 v219, v167 offset:5200
	s_waitcnt lgkmcnt(1)
	v_bfe_u32 v220, v218, 16, 1
	v_add3_u32 v218, v218, v220, s10
	s_waitcnt lgkmcnt(0)
	v_bfe_u32 v220, v219, 16, 1
	v_lshrrev_b32_e32 v218, 16, v218
	v_add3_u32 v219, v219, v220, s10
	v_and_or_b32 v218, v219, s11, v218
	ds_read_b32 v219, v167 offset:6240
	ds_read_b32 v220, v167 offset:7280
	s_waitcnt lgkmcnt(1)
	v_bfe_u32 v221, v219, 16, 1
	v_add3_u32 v219, v219, v221, s10
	s_waitcnt lgkmcnt(0)
	v_bfe_u32 v221, v220, 16, 1
	v_lshrrev_b32_e32 v219, 16, v219
	v_add3_u32 v220, v220, v221, s10
	v_and_or_b32 v219, v220, s11, v219
	v_ashrrev_i32_e32 v220, 31, v215
	v_mul_lo_u32 v222, s68, v220
	v_mad_u64_u32 v[220:221], s[0:1], s68, v215, 0
	v_add3_u32 v221, v221, v222, v223
	v_lshl_add_u64 v[220:221], v[220:221], 1, s[66:67]
	v_lshl_add_u64 v[220:221], v[220:221], 0, s[40:41]
	v_lshl_add_u64 v[220:221], v[220:221], 0, v[156:157]
	v_add_u32_e32 v215, s84, v166
	global_store_dwordx4 v[220:221], v[216:219], off
	s_nop 1
	v_lshlrev_b32_e32 v216, 1, v215
	v_and_b32_e32 v216, 0xffffff00, v216
	v_or3_b32 v216, v165, v216, s19
	v_cndmask_b32_e64 v215, v216, v215, s[72:73]
	ds_read_b32 v216, v164
	ds_read_b32 v217, v164 offset:1040
	v_mul_lo_u32 v223, s69, v215
	s_waitcnt lgkmcnt(1)
; #define GAS __attribute__((address_space(1)))
; #define LAS __attribute__((address_space(3)))
; __device__ __forceinline__ unsigned pk2(float lo, float hi) { return f2bf(lo) | (f2bf(hi) << 16); }
; __device__ __forceinline__ void cv_tile_out(const CvTile& cur, LAS float* S, int tid_) {
;     ...
; #pragma unroll
;         for (int i = 0; i < 8; ++i) { const int p = tid_ + 512 * i, kc = p & 15, n = p >> 4, nn = 256 * nb + n;
;             const int drow = (cur.mode == 0) ? nn : (256 * (nn >> 7) + (nn & 127) + (cur.mode == 2 ? 128 : 0));
;             const LAS float* sp = S + (8 * kc) * LS + (n ^ (4 * (kc >> 1))); v4u o;
;             o.x = pk2(sp[0], sp[LS]); o.y = pk2(sp[2 * LS], sp[3 * LS]); o.z = pk2(sp[4 * LS], sp[5 * LS]); o.w = pk2(sp[6 * LS], sp[7 * LS]);
;             *(GAS v4u*)((bf16*)cur.WT + (size_t)drow * cur.K + 128 * kb + 8 * kc) = o; } }
	v_bfe_u32 v218, v216, 16, 1
	v_add3_u32 v216, v216, v218, s10
	s_waitcnt lgkmcnt(0)
	v_bfe_u32 v218, v217, 16, 1
	v_lshrrev_b32_e32 v216, 16, v216
	v_add3_u32 v217, v217, v218, s10
	v_and_or_b32 v216, v217, s11, v216
	ds_read_b32 v217, v164 offset:2080
	ds_read_b32 v218, v164 offset:3120
	s_waitcnt lgkmcnt(1)
	v_bfe_u32 v219, v217, 16, 1
	v_add3_u32 v217, v217, v219, s10
	s_waitcnt lgkmcnt(0)
	v_bfe_u32 v219, v218, 16, 1
	v_lshrrev_b32_e32 v217, 16, v217
	v_add3_u32 v218, v218, v219, s10
	v_and_or_b32 v217, v218, s11, v217
	ds_read_b32 v218, v164 offset:4160
	ds_read_b32 v219, v164 offset:5200
	s_waitcnt lgkmcnt(1)
	v_bfe_u32 v220, v218, 16, 1
	v_add3_u32 v218, v218, v220, s10
	s_waitcnt lgkmcnt(0)
	v_bfe_u32 v220, v219, 16, 1
	v_lshrrev_b32_e32 v218, 16, v218
	v_add3_u32 v219, v219, v220, s10
	v_and_or_b32 v218, v219, s11, v218
	ds_read_b32 v219, v164 offset:6240
	ds_read_b32 v220, v164 offset:7280
	s_waitcnt lgkmcnt(1)
	v_bfe_u32 v221, v219, 16, 1
	v_add3_u32 v219, v219, v221, s10
	s_waitcnt lgkmcnt(0)
	v_bfe_u32 v221, v220, 16, 1
	v_lshrrev_b32_e32 v219, 16, v219
	v_add3_u32 v220, v220, v221, s10
	v_and_or_b32 v219, v220, s11, v219
	v_ashrrev_i32_e32 v220, 31, v215
	v_mul_lo_u32 v222, s68, v220
	v_mad_u64_u32 v[220:221], s[0:1], s68, v215, 0
	v_add3_u32 v221, v221, v222, v223
	v_lshl_add_u64 v[220:221], v[220:221], 1, s[66:67]
	v_lshl_add_u64 v[220:221], v[220:221], 0, s[40:41]
	v_lshl_add_u64 v[220:221], v[220:221], 0, v[156:157]
	v_add_u32_e32 v215, s84, v163
	global_store_dwordx4 v[220:221], v[216:219], off
	s_nop 1
	v_lshlrev_b32_e32 v216, 1, v215
	v_and_b32_e32 v216, 0xffffff00, v216
	v_or3_b32 v216, v162, v216, s19
	v_cndmask_b32_e64 v215, v216, v215, s[72:73]
	ds_read_b32 v216, v161
	ds_read_b32 v217, v161 offset:1040
	v_mul_lo_u32 v223, s69, v215
	s_waitcnt lgkmcnt(1)
	v_bfe_u32 v218, v216, 16, 1
	v_add3_u32 v216, v216, v218, s10
	s_waitcnt lgkmcnt(0)
	v_bfe_u32 v218, v217, 16, 1
	v_lshrrev_b32_e32 v216, 16, v216
	v_add3_u32 v217, v217, v218, s10
	v_and_or_b32 v216, v217, s11, v216
	ds_read_b32 v217, v161 offset:2080
	ds_read_b32 v218, v161 offset:3120
	s_waitcnt lgkmcnt(1)
	v_bfe_u32 v219, v217, 16, 1
	v_add3_u32 v217, v217, v219, s10
	s_waitcnt lgkmcnt(0)
	v_bfe_u32 v219, v218, 16, 1
	v_lshrrev_b32_e32 v217, 16, v217
	v_add3_u32 v218, v218, v219, s10
	v_and_or_b32 v217, v218, s11, v217
	ds_read_b32 v218, v161 offset:4160
	ds_read_b32 v219, v161 offset:5200
	s_waitcnt lgkmcnt(1)
	v_bfe_u32 v220, v218, 16, 1
	v_add3_u32 v218, v218, v220, s10
	s_waitcnt lgkmcnt(0)
	v_bfe_u32 v220, v219, 16, 1
	v_lshrrev_b32_e32 v218, 16, v218
	v_add3_u32 v219, v219, v220, s10
	v_and_or_b32 v218, v219, s11, v218
	ds_read_b32 v219, v161 offset:6240
	ds_read_b32 v220, v161 offset:7280
	s_waitcnt lgkmcnt(1)
	v_bfe_u32 v221, v219, 16, 1
	v_add3_u32 v219, v219, v221, s10
	s_waitcnt lgkmcnt(0)
	v_bfe_u32 v221, v220, 16, 1
	v_lshrrev_b32_e32 v219, 16, v219
	v_add3_u32 v220, v220, v221, s10
	v_and_or_b32 v219, v220, s11, v219
	v_ashrrev_i32_e32 v220, 31, v215
	v_mul_lo_u32 v222, s68, v220
	v_mad_u64_u32 v[220:221], s[0:1], s68, v215, 0
	v_add3_u32 v221, v221, v222, v223
	v_lshl_add_u64 v[220:221], v[220:221], 1, s[66:67]
	v_lshl_add_u64 v[220:221], v[220:221], 0, s[40:41]
	v_lshl_add_u64 v[220:221], v[220:221], 0, v[156:157]
	v_add_u32_e32 v215, s84, v160
	global_store_dwordx4 v[220:221], v[216:219], off
	s_nop 1
	v_lshlrev_b32_e32 v216, 1, v215
	v_and_b32_e32 v216, 0xffffff00, v216
	v_or3_b32 v216, v159, v216, s19
	v_cndmask_b32_e64 v215, v216, v215, s[72:73]
	ds_read_b32 v216, v158
	ds_read_b32 v217, v158 offset:1040
	v_mul_lo_u32 v223, s69, v215
	s_waitcnt lgkmcnt(1)
	v_bfe_u32 v218, v216, 16, 1
	v_add3_u32 v216, v216, v218, s10
	s_waitcnt lgkmcnt(0)
	v_bfe_u32 v218, v217, 16, 1
	v_lshrrev_b32_e32 v216, 16, v216
	v_add3_u32 v217, v217, v218, s10
	v_and_or_b32 v216, v217, s11, v216
	ds_read_b32 v217, v158 offset:2080
	ds_read_b32 v218, v158 offset:3120
	s_waitcnt lgkmcnt(1)
	v_bfe_u32 v219, v217, 16, 1
	v_add3_u32 v217, v217, v219, s10
	s_waitcnt lgkmcnt(0)
	v_bfe_u32 v219, v218, 16, 1
	v_lshrrev_b32_e32 v217, 16, v217
	v_add3_u32 v218, v218, v219, s10
	v_and_or_b32 v217, v218, s11, v217
	ds_read_b32 v218, v158 offset:4160
	ds_read_b32 v219, v158 offset:5200
	s_waitcnt lgkmcnt(1)
	v_bfe_u32 v220, v218, 16, 1
	v_add3_u32 v218, v218, v220, s10
	s_waitcnt lgkmcnt(0)
	v_bfe_u32 v220, v219, 16, 1
	v_lshrrev_b32_e32 v218, 16, v218
	v_add3_u32 v219, v219, v220, s10
	v_and_or_b32 v218, v219, s11, v218
	ds_read_b32 v219, v158 offset:6240
	ds_read_b32 v220, v158 offset:7280
	s_waitcnt lgkmcnt(1)
	v_bfe_u32 v221, v219, 16, 1
	v_add3_u32 v219, v219, v221, s10
	s_waitcnt lgkmcnt(0)
	v_bfe_u32 v221, v220, 16, 1
	v_lshrrev_b32_e32 v219, 16, v219
	v_add3_u32 v220, v220, v221, s10
	v_and_or_b32 v219, v220, s11, v219
	v_ashrrev_i32_e32 v220, 31, v215
	v_mul_lo_u32 v222, s68, v220
	v_mad_u64_u32 v[220:221], s[0:1], s68, v215, 0
	v_add3_u32 v221, v221, v222, v223
	v_lshl_add_u64 v[220:221], v[220:221], 1, s[66:67]
	v_lshl_add_u64 v[220:221], v[220:221], 0, s[40:41]
	v_lshl_add_u64 v[220:221], v[220:221], 0, v[156:157]
	global_store_dwordx4 v[220:221], v[216:219], off
	s_waitcnt lgkmcnt(0)
	s_mov_b64 s[0:1], -1
	s_barrier

; __device__ __forceinline__ unsigned pk4_fp8(float a, float b, float c, float d) { int w = 0; w = __builtin_amdgcn_cvt_pk_fp8_f32(a, b, w, false); w = __builtin_amdgcn_cvt_pk_fp8_f32(c, d, w, true); return (unsigned)w; }
; #define LAS __attribute__((address_space(3)))
; #define lane (lane_id())
; __device__ __forceinline__ void cv8_to_lds(const f32x4 (&v)[16], LAS unsigned char* T, int wave, int lane) {
;     unsigned d[16];
; #pragma unroll
;     for (int i = 0; i < 16; ++i) d[i] = pg8::pk4_fp8(v[i].x * 256.f, v[i].y * 256.f, v[i].z * 256.f, v[i].w * 256.f);
;     unsigned o[4][4];
; #pragma unroll
;     for (int q = 0; q < 4; ++q) { const unsigned a = d[4 * q], b = d[4 * q + 1], c = d[4 * q + 2], e = d[4 * q + 3];
;         const unsigned t0 = __builtin_amdgcn_perm(b, a, 0x05010400u), t1 = __builtin_amdgcn_perm(b, a, 0x07030602u), t2 = __builtin_amdgcn_perm(e, c, 0x05010400u), t3 = __builtin_amdgcn_perm(e, c, 0x07030602u);
;         o[0][q] = __builtin_amdgcn_perm(t2, t0, 0x05040100u); o[1][q] = __builtin_amdgcn_perm(t2, t0, 0x07060302u); o[2][q] = __builtin_amdgcn_perm(t3, t1, 0x05040100u); o[3][q] = __builtin_amdgcn_perm(t3, t1, 0x07060302u); }
; #pragma unroll
;     for (int j = 0; j < 4; ++j) { v4u w; w.x = o[j][0]; w.y = o[j][1]; w.z = o[j][2]; w.w = o[j][3];
;         *(LAS v4u*)(T + (4 * lane + j) * 128 + 16 * (wave ^ (lane & 7))) = w; }
; }
.Lpb2_491:
	s_xor_b64 s[28:29], s[74:75], -1
	v_readlane_b32 s48, v254, 38
	v_readlane_b32 s50, v254, 40
	v_readlane_b32 s52, v254, 42
	v_readlane_b32 s53, v254, 43
	s_mov_b64 s[0:1], -1
	s_and_b64 vcc, exec, s[28:29]
	v_readlane_b32 s49, v254, 39
	v_readlane_b32 s51, v254, 41
	s_cbranch_vccz .Lpb2_495
	s_waitcnt vmcnt(15)
	v_mul_f32_e32 v157, 0x43800000, v2
	v_mul_f32_e32 v215, 0x43800000, v3
	v_mov_b32_e32 v218, v1
	v_cvt_pk_fp8_f32 v218, v157, v215
	s_waitcnt vmcnt(14)
	v_mul_f32_e32 v157, 0x43800000, v6
	v_mul_f32_e32 v215, 0x43800000, v7
	v_mov_b32_e32 v219, v1
	v_cvt_pk_fp8_f32 v219, v157, v215
	v_mul_f32_e32 v157, 0x43800000, v8
	v_mul_f32_e32 v215, 0x43800000, v9
	v_mov_b32_e32 v220, v1
	v_cvt_pk_fp8_f32 v219, v157, v215 op_sel:[0,0,1]
	s_waitcnt vmcnt(13)
	v_mul_f32_e32 v157, 0x43800000, v10
	v_mul_f32_e32 v215, 0x43800000, v11
	v_cvt_pk_fp8_f32 v220, v157, v215
	s_waitcnt vmcnt(12)
	v_mul_f32_e32 v157, 0x43800000, v14
	v_mul_f32_e32 v215, 0x43800000, v15
	v_mov_b32_e32 v221, v1
	v_cvt_pk_fp8_f32 v221, v157, v215
	v_mul_f32_e32 v157, 0x43800000, v16
	v_mul_f32_e32 v215, 0x43800000, v17
	v_mov_b32_e32 v222, v1
	v_cvt_pk_fp8_f32 v221, v157, v215 op_sel:[0,0,1]
	s_waitcnt vmcnt(11)
	v_mul_f32_e32 v157, 0x43800000, v18
	v_mul_f32_e32 v215, 0x43800000, v19
	v_cvt_pk_fp8_f32 v222, v157, v215
	s_waitcnt vmcnt(10)
	v_mul_f32_e32 v157, 0x43800000, v22
	v_mul_f32_e32 v215, 0x43800000, v23
	v_mov_b32_e32 v223, v1
	v_cvt_pk_fp8_f32 v223, v157, v215
	v_mul_f32_e32 v157, 0x43800000, v24
	v_mul_f32_e32 v215, 0x43800000, v25
	v_mov_b32_e32 v225, v1
	v_cvt_pk_fp8_f32 v223, v157, v215 op_sel:[0,0,1]
	s_waitcnt vmcnt(9)
	v_mul_f32_e32 v157, 0x43800000, v26
	v_mul_f32_e32 v215, 0x43800000, v27
	v_cvt_pk_fp8_f32 v225, v157, v215
	s_waitcnt vmcnt(8)
	v_mul_f32_e32 v157, 0x43800000, v30
	v_mul_f32_e32 v215, 0x43800000, v31
	v_mov_b32_e32 v226, v1
	v_cvt_pk_fp8_f32 v226, v157, v215
	v_mul_f32_e32 v157, 0x43800000, v32
	v_mul_f32_e32 v215, 0x43800000, v33
	v_mov_b32_e32 v227, v1
	v_cvt_pk_fp8_f32 v226, v157, v215 op_sel:[0,0,1]
	s_waitcnt vmcnt(7)
	v_mul_f32_e32 v157, 0x43800000, v34
	v_mul_f32_e32 v215, 0x43800000, v35
	v_cvt_pk_fp8_f32 v227, v157, v215
	s_waitcnt vmcnt(6)
	v_mul_f32_e32 v157, 0x43800000, v38
	v_mul_f32_e32 v215, 0x43800000, v39
	v_mov_b32_e32 v230, v1
	v_cvt_pk_fp8_f32 v230, v157, v215
	v_mul_f32_e32 v157, 0x43800000, v40
	v_mul_f32_e32 v215, 0x43800000, v41
	v_mov_b32_e32 v231, v1
	v_cvt_pk_fp8_f32 v230, v157, v215 op_sel:[0,0,1]
	s_waitcnt vmcnt(5)
	v_mul_f32_e32 v157, 0x43800000, v42
	v_mul_f32_e32 v215, 0x43800000, v43
	v_cvt_pk_fp8_f32 v231, v157, v215
	s_waitcnt vmcnt(4)
	v_mul_f32_e32 v157, 0x43800000, v46
	v_mul_f32_e32 v215, 0x43800000, v47
	v_mov_b32_e32 v232, v1
	v_cvt_pk_fp8_f32 v232, v157, v215
	v_mul_f32_e32 v157, 0x43800000, v48
	v_mul_f32_e32 v215, 0x43800000, v49
	v_mov_b32_e32 v233, v1
	v_cvt_pk_fp8_f32 v232, v157, v215 op_sel:[0,0,1]
	s_waitcnt vmcnt(3)
	v_mul_f32_e32 v157, 0x43800000, v50
	v_mul_f32_e32 v215, 0x43800000, v51
	v_cvt_pk_fp8_f32 v233, v157, v215
	s_waitcnt vmcnt(2)
	v_mul_f32_e32 v157, 0x43800000, v54
	v_mul_f32_e32 v215, 0x43800000, v55
	v_mov_b32_e32 v234, v1
	v_cvt_pk_fp8_f32 v234, v157, v215
	v_mul_f32_e32 v216, 0x43800000, v4
	v_mul_f32_e32 v217, 0x43800000, v5
	v_cvt_pk_fp8_f32 v218, v216, v217 op_sel:[0,0,1]
	v_mul_f32_e32 v216, 0x43800000, v12
	v_mul_f32_e32 v217, 0x43800000, v13
	v_mul_f32_e32 v157, 0x43800000, v56
	v_mul_f32_e32 v215, 0x43800000, v57
	v_cvt_pk_fp8_f32 v220, v216, v217 op_sel:[0,0,1]
	v_mul_f32_e32 v216, 0x43800000, v20
	v_mul_f32_e32 v217, 0x43800000, v21
	v_cvt_pk_fp8_f32 v234, v157, v215 op_sel:[0,0,1]
	s_waitcnt vmcnt(1)
	v_mul_f32_e32 v157, 0x43800000, v58
	v_mul_f32_e32 v215, 0x43800000, v59
	v_mov_b32_e32 v235, v1
	v_cvt_pk_fp8_f32 v222, v216, v217 op_sel:[0,0,1]
	v_mul_f32_e32 v216, 0x43800000, v28
	v_mul_f32_e32 v217, 0x43800000, v29
	v_cvt_pk_fp8_f32 v235, v157, v215
	s_waitcnt vmcnt(0)
	v_mul_f32_e32 v157, 0x43800000, v62
	v_mul_f32_e32 v215, 0x43800000, v63
	v_mov_b32_e32 v236, v1
	v_cvt_pk_fp8_f32 v225, v216, v217 op_sel:[0,0,1]
	v_mul_f32_e32 v216, 0x43800000, v36
	v_mul_f32_e32 v217, 0x43800000, v37
	v_cvt_pk_fp8_f32 v236, v157, v215
	v_cvt_pk_fp8_f32 v227, v216, v217 op_sel:[0,0,1]
	v_mul_f32_e32 v216, 0x43800000, v44
	v_mul_f32_e32 v217, 0x43800000, v45
	v_cvt_pk_fp8_f32 v231, v216, v217 op_sel:[0,0,1]
	v_mul_f32_e32 v216, 0x43800000, v52
	v_mul_f32_e32 v217, 0x43800000, v53
	v_cvt_pk_fp8_f32 v233, v216, v217 op_sel:[0,0,1]
	v_mul_f32_e32 v216, 0x43800000, v60
	v_mul_f32_e32 v217, 0x43800000, v61
	v_mul_f32_e32 v157, 0x43800000, v64
	v_mul_f32_e32 v215, 0x43800000, v65
	v_cvt_pk_fp8_f32 v235, v216, v217 op_sel:[0,0,1]
	v_cvt_pk_fp8_f32 v236, v157, v215 op_sel:[0,0,1]
	s_mov_b32 s0, 0x5010400
	s_mov_b32 s1, 0x7030602
	v_perm_b32 v157, v219, v218, s0
	v_perm_b32 v215, v219, v218, s1
	v_perm_b32 v217, v221, v220, s0
	v_perm_b32 v218, v221, v220, s1
	s_mov_b32 s4, 0x5040100
	s_mov_b32 s3, 0x7060302
	v_perm_b32 v216, v217, v157, s4
	v_perm_b32 v220, v217, v157, s3
	v_perm_b32 v224, v218, v215, s4
	v_perm_b32 v228, v218, v215, s3
	v_perm_b32 v157, v223, v222, s0
	v_perm_b32 v215, v223, v222, s1
	v_perm_b32 v218, v226, v225, s0
	v_perm_b32 v219, v226, v225, s1
	v_perm_b32 v217, v218, v157, s4
	v_perm_b32 v221, v218, v157, s3
	v_perm_b32 v225, v219, v215, s4
	v_perm_b32 v229, v219, v215, s3
	v_perm_b32 v157, v230, v227, s0
	v_perm_b32 v215, v230, v227, s1
	v_perm_b32 v219, v232, v231, s0
	v_perm_b32 v223, v232, v231, s1
	v_perm_b32 v218, v219, v157, s4
	v_perm_b32 v222, v219, v157, s3
	v_perm_b32 v226, v223, v215, s4
	v_perm_b32 v230, v223, v215, s3
	v_perm_b32 v157, v234, v233, s0
	v_perm_b32 v223, v236, v235, s0
	v_perm_b32 v215, v234, v233, s1
	v_perm_b32 v231, v236, v235, s1
	v_perm_b32 v219, v223, v157, s4
	v_perm_b32 v223, v223, v157, s3
	v_add_u32_e32 v157, s22, v240
	v_perm_b32 v227, v231, v215, s4
	v_perm_b32 v231, v231, v215, s3
	ds_write_b128 v157, v[216:219]
	ds_write_b128 v157, v[220:223] offset:128
	ds_write_b128 v157, v[224:227] offset:256
	ds_write_b128 v157, v[228:231] offset:384
	s_waitcnt lgkmcnt(0)
	s_waitcnt lgkmcnt(0)
	s_barrier
	s_cbranch_execz .Lpb2_496

; #define GAS __attribute__((address_space(1)))
; #define LAS __attribute__((address_space(3)))
; __device__ __forceinline__ void cv8_out(const CvTile& cur, const LAS unsigned char* T, int tid_) {
;     const int nbl = cur.N / 256, kb = cur.r / nbl, nb = cur.r - kb * nbl;
; #pragma unroll
;     for (int i = 0; i < 4; ++i) { const int p = tid_ + 512 * i, c = p & 7, n = p >> 3, nn = 256 * nb + n;
;         const int drow = (cur.mode == 0) ? nn : (256 * (nn >> 7) + (nn & 127) + (cur.mode == 2 ? 128 : 0));
;         const v4u w = *(const LAS v4u*)(T + n * 128 + 16 * (c ^ ((n >> 2) & 7)));
;         __builtin_nontemporal_store(w, (GAS v4u*)(cur.WT + (size_t)drow * cur.K + 128 * kb + 16 * c)); }
; }
.Lpb2_494:
	s_waitcnt vmcnt(15)
	v_add_u32_e32 v2, s64, v212
	v_lshlrev_b32_e32 v3, 1, v2
	v_and_b32_e32 v3, 0xffffff00, v3
	v_or3_b32 v3, v210, v3, s18
	s_waitcnt vmcnt(13)
	v_add_u32_e32 v10, s22, v211
	v_cndmask_b32_e64 v8, v3, v2, s[62:63]
	v_add_u32_e32 v2, v10, v209
	v_ashrrev_i32_e32 v6, 31, v8
	ds_read_b128 v[2:5], v2
	v_mul_lo_u32 v11, s60, v6
	v_mov_b64_e32 v[6:7], s[58:59]
	v_mul_lo_u32 v12, s61, v8
	v_mad_u64_u32 v[8:9], s[0:1], s60, v8, v[6:7]
	s_ashr_i32 s71, s70, 31
	v_add3_u32 v9, v12, v9, v11
	v_lshl_add_u64 v[8:9], v[8:9], 0, s[70:71]
	v_lshl_add_u64 v[8:9], v[8:9], 0, v[0:1]
	s_waitcnt lgkmcnt(0)
	global_store_dwordx4 v[8:9], v[2:5], off nt
	s_nop 1
	v_add_u32_e32 v2, s64, v208
	v_lshlrev_b32_e32 v3, 1, v2
	v_and_b32_e32 v3, 0xffffff00, v3
	v_or3_b32 v3, v187, v3, s18
	v_cndmask_b32_e64 v8, v3, v2, s[62:63]
	v_add_u32_e32 v2, v10, v186
	ds_read_b128 v[2:5], v2
	v_ashrrev_i32_e32 v9, 31, v8
	v_mul_lo_u32 v11, s60, v9
	v_mul_lo_u32 v12, s61, v8
	v_mad_u64_u32 v[8:9], s[0:1], s60, v8, v[6:7]
	v_add3_u32 v9, v12, v9, v11
	v_lshl_add_u64 v[8:9], v[8:9], 0, s[70:71]
	v_lshl_add_u64 v[8:9], v[8:9], 0, v[0:1]
	s_waitcnt lgkmcnt(0)
	global_store_dwordx4 v[8:9], v[2:5], off nt
	s_nop 1
	v_add_u32_e32 v2, s64, v184
	v_lshlrev_b32_e32 v3, 1, v2
	v_and_b32_e32 v3, 0xffffff00, v3
	v_or3_b32 v3, v183, v3, s18
	v_cndmask_b32_e64 v8, v3, v2, s[62:63]
	v_add_u32_e32 v2, v10, v182
	ds_read_b128 v[2:5], v2
	v_ashrrev_i32_e32 v9, 31, v8
	v_mul_lo_u32 v11, s60, v9
	v_mul_lo_u32 v12, s61, v8
	v_mad_u64_u32 v[8:9], s[0:1], s60, v8, v[6:7]
	v_add3_u32 v9, v12, v9, v11
	v_lshl_add_u64 v[8:9], v[8:9], 0, s[70:71]
	v_lshl_add_u64 v[8:9], v[8:9], 0, v[0:1]
	s_waitcnt lgkmcnt(0)
	global_store_dwordx4 v[8:9], v[2:5], off nt
	s_nop 1
	v_add_u32_e32 v2, s64, v181
	v_lshlrev_b32_e32 v3, 1, v2
	v_and_b32_e32 v3, 0xffffff00, v3
	v_or3_b32 v3, v180, v3, s18
	v_cndmask_b32_e64 v8, v3, v2, s[62:63]
	v_add_u32_e32 v2, v10, v179
	ds_read_b128 v[2:5], v2
	v_ashrrev_i32_e32 v9, 31, v8
	v_mul_lo_u32 v9, s60, v9
	v_mul_lo_u32 v10, s61, v8
	v_mad_u64_u32 v[6:7], s[0:1], s60, v8, v[6:7]
	v_add3_u32 v7, v10, v7, v9
	v_lshl_add_u64 v[6:7], v[6:7], 0, s[70:71]
	v_lshl_add_u64 v[6:7], v[6:7], 0, v[0:1]
	s_waitcnt lgkmcnt(0)
	global_store_dwordx4 v[6:7], v[2:5], off nt
	s_waitcnt lgkmcnt(0)
	s_barrier
	s_cbranch_execz .Lpb2_498
	s_branch .LBB0_499

.Lpb2_496:
	s_waitcnt vmcnt(15)
	ds_write_b128 v241, v[2:5]
	s_waitcnt vmcnt(14)
	ds_write_b128 v241, v[6:9] offset:1040
	s_waitcnt vmcnt(13)
	ds_write_b128 v241, v[10:13] offset:2080
	s_waitcnt vmcnt(12)
	ds_write_b128 v241, v[14:17] offset:3120
	s_waitcnt vmcnt(11)
	ds_write_b128 v241, v[18:21] offset:4160
	s_waitcnt vmcnt(10)
	ds_write_b128 v241, v[22:25] offset:5200
	s_waitcnt vmcnt(9)
	ds_write_b128 v241, v[26:29] offset:6240
	s_waitcnt vmcnt(8)
	ds_write_b128 v241, v[30:33] offset:7280
	s_waitcnt vmcnt(7)
	ds_write_b128 v241, v[34:37] offset:8320
	s_waitcnt vmcnt(6)
	ds_write_b128 v241, v[38:41] offset:9360
	s_waitcnt vmcnt(5)
	ds_write_b128 v241, v[42:45] offset:10400
	s_waitcnt vmcnt(4)
	ds_write_b128 v241, v[46:49] offset:11440
	s_waitcnt vmcnt(3)
	ds_write_b128 v241, v[50:53] offset:12480
	s_waitcnt vmcnt(2)
	ds_write_b128 v241, v[54:57] offset:13520
	s_waitcnt vmcnt(1)
	ds_write_b128 v241, v[58:61] offset:14560
	s_waitcnt vmcnt(0)
	ds_write_b128 v241, v[62:65] offset:15600
	s_waitcnt lgkmcnt(0)
	s_waitcnt lgkmcnt(0)
	s_barrier
	s_andn2_b64 vcc, exec, s[28:29]
	s_mov_b64 s[0:1], -1
	s_cbranch_vccz .Lpb2_494

; #define GAS __attribute__((address_space(1)))
; #define LAS __attribute__((address_space(3)))
; __device__ __forceinline__ unsigned pk2(float lo, float hi) { return f2bf(lo) | (f2bf(hi) << 16); }
; __device__ __forceinline__ void cv_tile_out(const CvTile& cur, LAS float* S, int tid_) {
;     ...
; #pragma unroll
;         for (int i = 0; i < 8; ++i) { const int p = tid_ + 512 * i, kc = p & 15, n = p >> 4, nn = 256 * nb + n;
;             const int drow = (cur.mode == 0) ? nn : (256 * (nn >> 7) + (nn & 127) + (cur.mode == 2 ? 128 : 0));
;             const LAS float* sp = S + (8 * kc) * LS + (n ^ (4 * (kc >> 1))); v4u o;
;             o.x = pk2(sp[0], sp[LS]); o.y = pk2(sp[2 * LS], sp[3 * LS]); o.z = pk2(sp[4 * LS], sp[5 * LS]); o.w = pk2(sp[6 * LS], sp[7 * LS]);
;             *(GAS v4u*)((bf16*)cur.WT + (size_t)drow * cur.K + 128 * kb + 8 * kc) = o; } }
.Lpb2_498:
	v_add_u32_e32 v0, s64, v214
	s_waitcnt vmcnt(15)
	v_lshlrev_b32_e32 v2, 1, v0
	v_and_b32_e32 v2, 0xffffff00, v2
	v_or3_b32 v2, v213, v2, s18
	v_cndmask_b32_e64 v0, v2, v0, s[62:63]
	ds_read_b32 v2, v185
	ds_read_b32 v3, v185 offset:1040
	s_waitcnt vmcnt(14)
	v_mul_lo_u32 v9, s61, v0
	s_ashr_i32 s71, s70, 31
	s_lshl_b64 s[28:29], s[70:71], 1
	s_waitcnt lgkmcnt(1)
	v_bfe_u32 v4, v2, 16, 1
	v_add3_u32 v2, v2, v4, s10
	s_waitcnt lgkmcnt(0)
	v_bfe_u32 v4, v3, 16, 1
	v_lshrrev_b32_e32 v2, 16, v2
	v_add3_u32 v3, v3, v4, s10
	v_and_or_b32 v2, v3, s11, v2
	ds_read_b32 v3, v185 offset:2080
	ds_read_b32 v4, v185 offset:3120
	v_mov_b32_e32 v157, v1
	s_waitcnt lgkmcnt(1)
	v_bfe_u32 v5, v3, 16, 1
	v_add3_u32 v3, v3, v5, s10
	s_waitcnt lgkmcnt(0)
	v_bfe_u32 v5, v4, 16, 1
	v_lshrrev_b32_e32 v3, 16, v3
	v_add3_u32 v4, v4, v5, s10
	v_and_or_b32 v3, v4, s11, v3
	ds_read_b32 v4, v185 offset:4160
	ds_read_b32 v5, v185 offset:5200
	s_waitcnt lgkmcnt(1)
	v_bfe_u32 v6, v4, 16, 1
	v_add3_u32 v4, v4, v6, s10
	s_waitcnt lgkmcnt(0)
	v_bfe_u32 v6, v5, 16, 1
	v_lshrrev_b32_e32 v4, 16, v4
	v_add3_u32 v5, v5, v6, s10
	v_and_or_b32 v4, v5, s11, v4
	ds_read_b32 v5, v185 offset:6240
	ds_read_b32 v6, v185 offset:7280
	s_waitcnt lgkmcnt(1)
	v_bfe_u32 v7, v5, 16, 1
	v_add3_u32 v5, v5, v7, s10
	s_waitcnt lgkmcnt(0)
	v_bfe_u32 v7, v6, 16, 1
	v_lshrrev_b32_e32 v5, 16, v5
	v_add3_u32 v6, v6, v7, s10
	v_and_or_b32 v5, v6, s11, v5
	v_ashrrev_i32_e32 v6, 31, v0
	v_mul_lo_u32 v8, s60, v6
	v_mad_u64_u32 v[6:7], s[0:1], s60, v0, 0
	v_add3_u32 v7, v7, v8, v9
	v_lshl_add_u64 v[6:7], v[6:7], 1, s[58:59]
	v_lshl_add_u64 v[6:7], v[6:7], 0, s[28:29]
	v_lshl_add_u64 v[6:7], v[6:7], 0, v[156:157]
	v_add_u32_e32 v0, s64, v178
	global_store_dwordx4 v[6:7], v[2:5], off
	s_nop 1
	v_lshlrev_b32_e32 v2, 1, v0
	v_and_b32_e32 v2, 0xffffff00, v2
	v_or3_b32 v2, v177, v2, s18
	v_cndmask_b32_e64 v0, v2, v0, s[62:63]
	ds_read_b32 v2, v176
	ds_read_b32 v3, v176 offset:1040
	v_mul_lo_u32 v9, s61, v0
	s_waitcnt lgkmcnt(1)
	v_bfe_u32 v4, v2, 16, 1
	v_add3_u32 v2, v2, v4, s10
	s_waitcnt lgkmcnt(0)
	v_bfe_u32 v4, v3, 16, 1
	v_lshrrev_b32_e32 v2, 16, v2
	v_add3_u32 v3, v3, v4, s10
	v_and_or_b32 v2, v3, s11, v2
	ds_read_b32 v3, v176 offset:2080
	ds_read_b32 v4, v176 offset:3120
	s_waitcnt lgkmcnt(1)
	v_bfe_u32 v5, v3, 16, 1
	v_add3_u32 v3, v3, v5, s10
	s_waitcnt lgkmcnt(0)
	v_bfe_u32 v5, v4, 16, 1
	v_lshrrev_b32_e32 v3, 16, v3
	v_add3_u32 v4, v4, v5, s10
	v_and_or_b32 v3, v4, s11, v3
	ds_read_b32 v4, v176 offset:4160
	ds_read_b32 v5, v176 offset:5200
	s_waitcnt lgkmcnt(1)
	v_bfe_u32 v6, v4, 16, 1
	v_add3_u32 v4, v4, v6, s10
	s_waitcnt lgkmcnt(0)
	v_bfe_u32 v6, v5, 16, 1
	v_lshrrev_b32_e32 v4, 16, v4
	v_add3_u32 v5, v5, v6, s10
	v_and_or_b32 v4, v5, s11, v4
	ds_read_b32 v5, v176 offset:6240
	ds_read_b32 v6, v176 offset:7280
	s_waitcnt lgkmcnt(1)
	v_bfe_u32 v7, v5, 16, 1
	v_add3_u32 v5, v5, v7, s10
	s_waitcnt lgkmcnt(0)
	v_bfe_u32 v7, v6, 16, 1
	v_lshrrev_b32_e32 v5, 16, v5
	v_add3_u32 v6, v6, v7, s10
	v_and_or_b32 v5, v6, s11, v5
	v_ashrrev_i32_e32 v6, 31, v0
	v_mul_lo_u32 v8, s60, v6
	v_mad_u64_u32 v[6:7], s[0:1], s60, v0, 0
	v_add3_u32 v7, v7, v8, v9
	v_lshl_add_u64 v[6:7], v[6:7], 1, s[58:59]
	v_lshl_add_u64 v[6:7], v[6:7], 0, s[28:29]
	v_lshl_add_u64 v[6:7], v[6:7], 0, v[156:157]
	v_add_u32_e32 v0, s64, v175
	global_store_dwordx4 v[6:7], v[2:5], off
	s_nop 1
	v_lshlrev_b32_e32 v2, 1, v0
	v_and_b32_e32 v2, 0xffffff00, v2
	v_or3_b32 v2, v174, v2, s18
	v_cndmask_b32_e64 v0, v2, v0, s[62:63]
	ds_read_b32 v2, v173
	ds_read_b32 v3, v173 offset:1040
	v_mul_lo_u32 v9, s61, v0
	s_waitcnt lgkmcnt(1)
	v_bfe_u32 v4, v2, 16, 1
	v_add3_u32 v2, v2, v4, s10
	s_waitcnt lgkmcnt(0)
	v_bfe_u32 v4, v3, 16, 1
	v_lshrrev_b32_e32 v2, 16, v2
	v_add3_u32 v3, v3, v4, s10
	v_and_or_b32 v2, v3, s11, v2
	ds_read_b32 v3, v173 offset:2080
	ds_read_b32 v4, v173 offset:3120
	s_waitcnt lgkmcnt(1)
	v_bfe_u32 v5, v3, 16, 1
	v_add3_u32 v3, v3, v5, s10
	s_waitcnt lgkmcnt(0)
	v_bfe_u32 v5, v4, 16, 1
	v_lshrrev_b32_e32 v3, 16, v3
	v_add3_u32 v4, v4, v5, s10
	v_and_or_b32 v3, v4, s11, v3
	ds_read_b32 v4, v173 offset:4160
	ds_read_b32 v5, v173 offset:5200
	s_waitcnt lgkmcnt(1)
	v_bfe_u32 v6, v4, 16, 1
	v_add3_u32 v4, v4, v6, s10
	s_waitcnt lgkmcnt(0)
	v_bfe_u32 v6, v5, 16, 1
	v_lshrrev_b32_e32 v4, 16, v4
	v_add3_u32 v5, v5, v6, s10
	v_and_or_b32 v4, v5, s11, v4
	ds_read_b32 v5, v173 offset:6240
	ds_read_b32 v6, v173 offset:7280
	s_waitcnt lgkmcnt(1)
	v_bfe_u32 v7, v5, 16, 1
	v_add3_u32 v5, v5, v7, s10
	s_waitcnt lgkmcnt(0)
	v_bfe_u32 v7, v6, 16, 1
	v_lshrrev_b32_e32 v5, 16, v5
	v_add3_u32 v6, v6, v7, s10
	v_and_or_b32 v5, v6, s11, v5
	v_ashrrev_i32_e32 v6, 31, v0
	v_mul_lo_u32 v8, s60, v6
	v_mad_u64_u32 v[6:7], s[0:1], s60, v0, 0
	v_add3_u32 v7, v7, v8, v9
	v_lshl_add_u64 v[6:7], v[6:7], 1, s[58:59]
	v_lshl_add_u64 v[6:7], v[6:7], 0, s[28:29]
	v_lshl_add_u64 v[6:7], v[6:7], 0, v[156:157]
	v_add_u32_e32 v0, s64, v172
	global_store_dwordx4 v[6:7], v[2:5], off
	s_nop 1
	v_lshlrev_b32_e32 v2, 1, v0
	v_and_b32_e32 v2, 0xffffff00, v2
	v_or3_b32 v2, v171, v2, s18
	v_cndmask_b32_e64 v0, v2, v0, s[62:63]
	ds_read_b32 v2, v170
	ds_read_b32 v3, v170 offset:1040
	v_mul_lo_u32 v9, s61, v0
	s_waitcnt lgkmcnt(1)
	v_bfe_u32 v4, v2, 16, 1
	v_add3_u32 v2, v2, v4, s10
	s_waitcnt lgkmcnt(0)
	v_bfe_u32 v4, v3, 16, 1
	v_lshrrev_b32_e32 v2, 16, v2
	v_add3_u32 v3, v3, v4, s10
	v_and_or_b32 v2, v3, s11, v2
	ds_read_b32 v3, v170 offset:2080
	ds_read_b32 v4, v170 offset:3120
	s_waitcnt lgkmcnt(1)
	v_bfe_u32 v5, v3, 16, 1
	v_add3_u32 v3, v3, v5, s10
	s_waitcnt lgkmcnt(0)
; #define GAS __attribute__((address_space(1)))
; #define LAS __attribute__((address_space(3)))
; __device__ __forceinline__ unsigned pk2(float lo, float hi) { return f2bf(lo) | (f2bf(hi) << 16); }
; __device__ __forceinline__ void cv_tile_out(const CvTile& cur, LAS float* S, int tid_) {
;     ...
; #pragma unroll
;         for (int i = 0; i < 8; ++i) { const int p = tid_ + 512 * i, kc = p & 15, n = p >> 4, nn = 256 * nb + n;
;             const int drow = (cur.mode == 0) ? nn : (256 * (nn >> 7) + (nn & 127) + (cur.mode == 2 ? 128 : 0));
;             const LAS float* sp = S + (8 * kc) * LS + (n ^ (4 * (kc >> 1))); v4u o;
;             o.x = pk2(sp[0], sp[LS]); o.y = pk2(sp[2 * LS], sp[3 * LS]); o.z = pk2(sp[4 * LS], sp[5 * LS]); o.w = pk2(sp[6 * LS], sp[7 * LS]);
;             *(GAS v4u*)((bf16*)cur.WT + (size_t)drow * cur.K + 128 * kb + 8 * kc) = o; } }
	v_bfe_u32 v5, v4, 16, 1
	v_lshrrev_b32_e32 v3, 16, v3
	v_add3_u32 v4, v4, v5, s10
	v_and_or_b32 v3, v4, s11, v3
	ds_read_b32 v4, v170 offset:4160
	ds_read_b32 v5, v170 offset:5200
	s_waitcnt lgkmcnt(1)
	v_bfe_u32 v6, v4, 16, 1
	v_add3_u32 v4, v4, v6, s10
	s_waitcnt lgkmcnt(0)
	v_bfe_u32 v6, v5, 16, 1
	v_lshrrev_b32_e32 v4, 16, v4
	v_add3_u32 v5, v5, v6, s10
	v_and_or_b32 v4, v5, s11, v4
	ds_read_b32 v5, v170 offset:6240
	ds_read_b32 v6, v170 offset:7280
	s_waitcnt lgkmcnt(1)
	v_bfe_u32 v7, v5, 16, 1
	v_add3_u32 v5, v5, v7, s10
	s_waitcnt lgkmcnt(0)
	v_bfe_u32 v7, v6, 16, 1
	v_lshrrev_b32_e32 v5, 16, v5
	v_add3_u32 v6, v6, v7, s10
	v_and_or_b32 v5, v6, s11, v5
	v_ashrrev_i32_e32 v6, 31, v0
	v_mul_lo_u32 v8, s60, v6
	v_mad_u64_u32 v[6:7], s[0:1], s60, v0, 0
	v_add3_u32 v7, v7, v8, v9
	v_lshl_add_u64 v[6:7], v[6:7], 1, s[58:59]
	v_lshl_add_u64 v[6:7], v[6:7], 0, s[28:29]
	v_lshl_add_u64 v[6:7], v[6:7], 0, v[156:157]
	v_add_u32_e32 v0, s64, v169
	global_store_dwordx4 v[6:7], v[2:5], off
	s_nop 1
	v_lshlrev_b32_e32 v2, 1, v0
	v_and_b32_e32 v2, 0xffffff00, v2
	v_or3_b32 v2, v168, v2, s18
	v_cndmask_b32_e64 v0, v2, v0, s[62:63]
	ds_read_b32 v2, v167
	ds_read_b32 v3, v167 offset:1040
	v_mul_lo_u32 v9, s61, v0
	s_waitcnt lgkmcnt(1)
	v_bfe_u32 v4, v2, 16, 1
	v_add3_u32 v2, v2, v4, s10
	s_waitcnt lgkmcnt(0)
	v_bfe_u32 v4, v3, 16, 1
	v_lshrrev_b32_e32 v2, 16, v2
	v_add3_u32 v3, v3, v4, s10
	v_and_or_b32 v2, v3, s11, v2
	ds_read_b32 v3, v167 offset:2080
	ds_read_b32 v4, v167 offset:3120
	s_waitcnt lgkmcnt(1)
	v_bfe_u32 v5, v3, 16, 1
	v_add3_u32 v3, v3, v5, s10
	s_waitcnt lgkmcnt(0)
	v_bfe_u32 v5, v4, 16, 1
	v_lshrrev_b32_e32 v3, 16, v3
	v_add3_u32 v4, v4, v5, s10
	v_and_or_b32 v3, v4, s11, v3
	ds_read_b32 v4, v167 offset:4160
	ds_read_b32 v5, v167 offset:5200
	s_waitcnt lgkmcnt(1)
	v_bfe_u32 v6, v4, 16, 1
	v_add3_u32 v4, v4, v6, s10
	s_waitcnt lgkmcnt(0)
	v_bfe_u32 v6, v5, 16, 1
	v_lshrrev_b32_e32 v4, 16, v4
	v_add3_u32 v5, v5, v6, s10
	v_and_or_b32 v4, v5, s11, v4
	ds_read_b32 v5, v167 offset:6240
	ds_read_b32 v6, v167 offset:7280
	s_waitcnt lgkmcnt(1)
	v_bfe_u32 v7, v5, 16, 1
	v_add3_u32 v5, v5, v7, s10
	s_waitcnt lgkmcnt(0)
	v_bfe_u32 v7, v6, 16, 1
	v_lshrrev_b32_e32 v5, 16, v5
	v_add3_u32 v6, v6, v7, s10
	v_and_or_b32 v5, v6, s11, v5
	v_ashrrev_i32_e32 v6, 31, v0
	v_mul_lo_u32 v8, s60, v6
	v_mad_u64_u32 v[6:7], s[0:1], s60, v0, 0
	v_add3_u32 v7, v7, v8, v9
	v_lshl_add_u64 v[6:7], v[6:7], 1, s[58:59]
	v_lshl_add_u64 v[6:7], v[6:7], 0, s[28:29]
	v_lshl_add_u64 v[6:7], v[6:7], 0, v[156:157]
	v_add_u32_e32 v0, s64, v166
	global_store_dwordx4 v[6:7], v[2:5], off
	s_nop 1
	v_lshlrev_b32_e32 v2, 1, v0
	v_and_b32_e32 v2, 0xffffff00, v2
	v_or3_b32 v2, v165, v2, s18
	v_cndmask_b32_e64 v0, v2, v0, s[62:63]
	ds_read_b32 v2, v164
	ds_read_b32 v3, v164 offset:1040
	v_mul_lo_u32 v9, s61, v0
	s_waitcnt lgkmcnt(1)
	v_bfe_u32 v4, v2, 16, 1
	v_add3_u32 v2, v2, v4, s10
	s_waitcnt lgkmcnt(0)
	v_bfe_u32 v4, v3, 16, 1
	v_lshrrev_b32_e32 v2, 16, v2
	v_add3_u32 v3, v3, v4, s10
	v_and_or_b32 v2, v3, s11, v2
	ds_read_b32 v3, v164 offset:2080
	ds_read_b32 v4, v164 offset:3120
	s_waitcnt lgkmcnt(1)
	v_bfe_u32 v5, v3, 16, 1
	v_add3_u32 v3, v3, v5, s10
	s_waitcnt lgkmcnt(0)
	v_bfe_u32 v5, v4, 16, 1
	v_lshrrev_b32_e32 v3, 16, v3
	v_add3_u32 v4, v4, v5, s10
	v_and_or_b32 v3, v4, s11, v3
	ds_read_b32 v4, v164 offset:4160
	ds_read_b32 v5, v164 offset:5200
	s_waitcnt lgkmcnt(1)
	v_bfe_u32 v6, v4, 16, 1
	v_add3_u32 v4, v4, v6, s10
	s_waitcnt lgkmcnt(0)
	v_bfe_u32 v6, v5, 16, 1
	v_lshrrev_b32_e32 v4, 16, v4
	v_add3_u32 v5, v5, v6, s10
	v_and_or_b32 v4, v5, s11, v4
	ds_read_b32 v5, v164 offset:6240
	ds_read_b32 v6, v164 offset:7280
	s_waitcnt lgkmcnt(1)
; #define GAS __attribute__((address_space(1)))
; #define LAS __attribute__((address_space(3)))
; __device__ __forceinline__ unsigned pk2(float lo, float hi) { return f2bf(lo) | (f2bf(hi) << 16); }
; __device__ __forceinline__ void cv_tile_out(const CvTile& cur, LAS float* S, int tid_) {
;     ...
; #pragma unroll
;         for (int i = 0; i < 8; ++i) { const int p = tid_ + 512 * i, kc = p & 15, n = p >> 4, nn = 256 * nb + n;
;             const int drow = (cur.mode == 0) ? nn : (256 * (nn >> 7) + (nn & 127) + (cur.mode == 2 ? 128 : 0));
;             const LAS float* sp = S + (8 * kc) * LS + (n ^ (4 * (kc >> 1))); v4u o;
;             o.x = pk2(sp[0], sp[LS]); o.y = pk2(sp[2 * LS], sp[3 * LS]); o.z = pk2(sp[4 * LS], sp[5 * LS]); o.w = pk2(sp[6 * LS], sp[7 * LS]);
;             *(GAS v4u*)((bf16*)cur.WT + (size_t)drow * cur.K + 128 * kb + 8 * kc) = o; } }
	v_bfe_u32 v7, v5, 16, 1
	v_add3_u32 v5, v5, v7, s10
	s_waitcnt lgkmcnt(0)
	v_bfe_u32 v7, v6, 16, 1
	v_lshrrev_b32_e32 v5, 16, v5
	v_add3_u32 v6, v6, v7, s10
	v_and_or_b32 v5, v6, s11, v5
	v_ashrrev_i32_e32 v6, 31, v0
	v_mul_lo_u32 v8, s60, v6
	v_mad_u64_u32 v[6:7], s[0:1], s60, v0, 0
	v_add3_u32 v7, v7, v8, v9
	v_lshl_add_u64 v[6:7], v[6:7], 1, s[58:59]
	v_lshl_add_u64 v[6:7], v[6:7], 0, s[28:29]
	v_lshl_add_u64 v[6:7], v[6:7], 0, v[156:157]
	v_add_u32_e32 v0, s64, v163
	global_store_dwordx4 v[6:7], v[2:5], off
	s_nop 1
	v_lshlrev_b32_e32 v2, 1, v0
	v_and_b32_e32 v2, 0xffffff00, v2
	v_or3_b32 v2, v162, v2, s18
	v_cndmask_b32_e64 v0, v2, v0, s[62:63]
	ds_read_b32 v2, v161
	ds_read_b32 v3, v161 offset:1040
	v_mul_lo_u32 v9, s61, v0
	s_waitcnt lgkmcnt(1)
	v_bfe_u32 v4, v2, 16, 1
	v_add3_u32 v2, v2, v4, s10
	s_waitcnt lgkmcnt(0)
	v_bfe_u32 v4, v3, 16, 1
	v_lshrrev_b32_e32 v2, 16, v2
	v_add3_u32 v3, v3, v4, s10
	v_and_or_b32 v2, v3, s11, v2
	ds_read_b32 v3, v161 offset:2080
	ds_read_b32 v4, v161 offset:3120
	s_waitcnt lgkmcnt(1)
	v_bfe_u32 v5, v3, 16, 1
	v_add3_u32 v3, v3, v5, s10
	s_waitcnt lgkmcnt(0)
	v_bfe_u32 v5, v4, 16, 1
	v_lshrrev_b32_e32 v3, 16, v3
	v_add3_u32 v4, v4, v5, s10
	v_and_or_b32 v3, v4, s11, v3
	ds_read_b32 v4, v161 offset:4160
	ds_read_b32 v5, v161 offset:5200
	s_waitcnt lgkmcnt(1)
	v_bfe_u32 v6, v4, 16, 1
	v_add3_u32 v4, v4, v6, s10
	s_waitcnt lgkmcnt(0)
	v_bfe_u32 v6, v5, 16, 1
	v_lshrrev_b32_e32 v4, 16, v4
	v_add3_u32 v5, v5, v6, s10
	v_and_or_b32 v4, v5, s11, v4
	ds_read_b32 v5, v161 offset:6240
	ds_read_b32 v6, v161 offset:7280
	s_waitcnt lgkmcnt(1)
	v_bfe_u32 v7, v5, 16, 1
	v_add3_u32 v5, v5, v7, s10
	s_waitcnt lgkmcnt(0)
	v_bfe_u32 v7, v6, 16, 1
	v_lshrrev_b32_e32 v5, 16, v5
	v_add3_u32 v6, v6, v7, s10
	v_and_or_b32 v5, v6, s11, v5
	v_ashrrev_i32_e32 v6, 31, v0
	v_mul_lo_u32 v8, s60, v6
	v_mad_u64_u32 v[6:7], s[0:1], s60, v0, 0
	v_add3_u32 v7, v7, v8, v9
	v_lshl_add_u64 v[6:7], v[6:7], 1, s[58:59]
	v_lshl_add_u64 v[6:7], v[6:7], 0, s[28:29]
	v_lshl_add_u64 v[6:7], v[6:7], 0, v[156:157]
	v_add_u32_e32 v0, s64, v160
	global_store_dwordx4 v[6:7], v[2:5], off
	s_nop 1
	v_lshlrev_b32_e32 v2, 1, v0
	v_and_b32_e32 v2, 0xffffff00, v2
	v_or3_b32 v2, v159, v2, s18
	v_cndmask_b32_e64 v0, v2, v0, s[62:63]
	ds_read_b32 v2, v158
	ds_read_b32 v3, v158 offset:1040
	v_mul_lo_u32 v9, s61, v0
	s_waitcnt lgkmcnt(1)
	v_bfe_u32 v4, v2, 16, 1
	v_add3_u32 v2, v2, v4, s10
	s_waitcnt lgkmcnt(0)
	v_bfe_u32 v4, v3, 16, 1
	v_lshrrev_b32_e32 v2, 16, v2
	v_add3_u32 v3, v3, v4, s10
	v_and_or_b32 v2, v3, s11, v2
	ds_read_b32 v3, v158 offset:2080
	ds_read_b32 v4, v158 offset:3120
	s_waitcnt lgkmcnt(1)
	v_bfe_u32 v5, v3, 16, 1
	v_add3_u32 v3, v3, v5, s10
	s_waitcnt lgkmcnt(0)
	v_bfe_u32 v5, v4, 16, 1
	v_lshrrev_b32_e32 v3, 16, v3
	v_add3_u32 v4, v4, v5, s10
	v_and_or_b32 v3, v4, s11, v3
	ds_read_b32 v4, v158 offset:4160
	ds_read_b32 v5, v158 offset:5200
	s_waitcnt lgkmcnt(1)
	v_bfe_u32 v6, v4, 16, 1
	v_add3_u32 v4, v4, v6, s10
	s_waitcnt lgkmcnt(0)
	v_bfe_u32 v6, v5, 16, 1
	v_lshrrev_b32_e32 v4, 16, v4
	v_add3_u32 v5, v5, v6, s10
	v_and_or_b32 v4, v5, s11, v4
	ds_read_b32 v5, v158 offset:6240
	ds_read_b32 v6, v158 offset:7280
	s_waitcnt lgkmcnt(1)
	v_bfe_u32 v7, v5, 16, 1
	v_add3_u32 v5, v5, v7, s10
	s_waitcnt lgkmcnt(0)
	v_bfe_u32 v7, v6, 16, 1
	v_lshrrev_b32_e32 v5, 16, v5
	v_add3_u32 v6, v6, v7, s10
	v_and_or_b32 v5, v6, s11, v5
	v_ashrrev_i32_e32 v6, 31, v0
	v_mul_lo_u32 v8, s60, v6
	v_mad_u64_u32 v[6:7], s[0:1], s60, v0, 0
	v_add3_u32 v7, v7, v8, v9
	v_lshl_add_u64 v[6:7], v[6:7], 1, s[58:59]
	v_lshl_add_u64 v[6:7], v[6:7], 0, s[28:29]
	v_lshl_add_u64 v[6:7], v[6:7], 0, v[156:157]
	global_store_dwordx4 v[6:7], v[2:5], off
	s_waitcnt lgkmcnt(0)
	s_barrier
